# v59 + code placement: the twelve fused fp8 loop heads aligned to 64 bytes
# baseline (speedup 1.0000x reference)
; #define PG8_STAGE(bufoff, gbase, voff) do { _Pragma("unroll") for (int _i = 0; _i < 2; ++_i) \
;         __builtin_amdgcn_global_load_lds((const unsigned*)((const char*)(gbase) + (voff)[_i]), (PG8_LAS unsigned*)(lds + (bufoff) + ldsw + _i * 8192), 16, 0, 0); } while (0)
; #define PG8_WAIT_V(n) asm volatile("s_waitcnt vmcnt(" #n ")" ::: "memory")
; #define PG8_WAIT_L(n) asm volatile("s_waitcnt lgkmcnt(" #n ")" ::: "memory")
; #define PG8_BAR __builtin_amdgcn_s_barrier()
; #define PG8_SCHED __builtin_amdgcn_sched_barrier(0)
; template <class Epi, class Sched, bool ALIGN_EPI = true, bool F8 = false>
; __device__ __forceinline__ void gemm_phase(PG8_LAS unsigned char* lds, const Sched& S, const Epi& E) {
;     ...
;             PG8_LDB(B0, 0, 0); PG8_LDB(B1, 0, 1); PG8_SCHED; PG8_LDA(At, 0, 0); PG8_STAGE(PG8_SA(1, 1), a1, voffA[1]);
;             PG8_WAIT_V(8); PG8_WAIT_L(0); PG8_BAR; PG8_MMA(0, 0, At, B0); PG8_MMA(0, 1, At, B1); PG8_BAR; PG8_SCHED;
;             PG8_LDA(At, 0, 1); PG8_STAGE(PG8_SB(0, 0), b2, voffB[0]); PG8_STAGE(PG8_SB(0, 1), b2, voffB[1]); PG8_STAGE(PG8_SA(0, 0), a2, vA2[0]);
;             PG8_WAIT_V(8); PG8_WAIT_L(0); PG8_BAR; PG8_MMA(1, 0, At, B0); PG8_MMA(1, 1, At, B1); PG8_BAR; PG8_SCHED;
;     ...
; #pragma unroll
;         for (int a = 0; a < 2; ++a)
; #pragma unroll
;             for (int b = 0; b < 2; ++b)
; #pragma unroll
;                 for (int m = 0; m < 4; ++m)
; #pragma unroll
;                     for (int n = 0; n < 2; ++n) acc[a][b][m][n] = (f32x4){0.f, 0.f, 0.f, 0.f};
;         }
;         cur = nxt; cA = nA; cB = nB; ++ui;
; #pragma unroll
;         for (int h = 0; h < 2; ++h)
; #pragma unroll
;             for (int i = 0; i < 2; ++i) voffA[h][i] = voffAn[h][i];
.LBB0_371:
	s_add_u32 s5, s28, 0x10000
	s_addc_u32 s19, s29, 0
	s_add_u32 s26, s26, 0x8000
	v_mov_b64_e32 v[34:35], 0
	s_addc_u32 s27, s27, 0
	s_mov_b32 s21, -2
	v_mov_b64_e32 v[36:37], 0
	v_mov_b64_e32 v[38:39], 0
	v_mov_b64_e32 v[40:41], 0
	v_mov_b64_e32 v[50:51], 0
	v_mov_b64_e32 v[52:53], 0
	v_mov_b64_e32 v[54:55], 0
	v_mov_b64_e32 v[56:57], 0
	v_mov_b64_e32 v[66:67], 0
	v_mov_b64_e32 v[68:69], 0
	v_mov_b64_e32 v[70:71], 0
	v_mov_b64_e32 v[72:73], 0
	v_mov_b64_e32 v[82:83], 0
	v_mov_b64_e32 v[84:85], 0
	v_mov_b64_e32 v[86:87], 0
	v_mov_b64_e32 v[88:89], 0
	v_mov_b64_e32 v[42:43], 0
	v_mov_b64_e32 v[44:45], 0
	v_mov_b64_e32 v[46:47], 0
	v_mov_b64_e32 v[48:49], 0
	v_mov_b64_e32 v[58:59], 0
	v_mov_b64_e32 v[60:61], 0
	v_mov_b64_e32 v[62:63], 0
	v_mov_b64_e32 v[64:65], 0
	v_mov_b64_e32 v[74:75], 0
	v_mov_b64_e32 v[76:77], 0
	v_mov_b64_e32 v[78:79], 0
	v_mov_b64_e32 v[80:81], 0
	v_mov_b64_e32 v[90:91], 0
	v_mov_b64_e32 v[92:93], 0
	v_mov_b64_e32 v[94:95], 0
	v_mov_b64_e32 v[96:97], 0
	v_mov_b64_e32 v[98:99], 0
	v_mov_b64_e32 v[100:101], 0
	v_mov_b64_e32 v[102:103], 0
	v_mov_b64_e32 v[104:105], 0
	v_mov_b64_e32 v[114:115], 0
	v_mov_b64_e32 v[116:117], 0
	v_mov_b64_e32 v[118:119], 0
	v_mov_b64_e32 v[120:121], 0
	v_mov_b64_e32 v[130:131], 0
	v_mov_b64_e32 v[132:133], 0
	v_mov_b64_e32 v[134:135], 0
	v_mov_b64_e32 v[136:137], 0
	v_mov_b64_e32 v[146:147], 0
	v_mov_b64_e32 v[148:149], 0
	v_mov_b64_e32 v[150:151], 0
	v_mov_b64_e32 v[152:153], 0
	v_mov_b64_e32 v[106:107], 0
	v_mov_b64_e32 v[108:109], 0
	v_mov_b64_e32 v[110:111], 0
	v_mov_b64_e32 v[112:113], 0
	v_mov_b64_e32 v[122:123], 0
	v_mov_b64_e32 v[124:125], 0
	v_mov_b64_e32 v[126:127], 0
	v_mov_b64_e32 v[128:129], 0
	v_mov_b64_e32 v[138:139], 0
	v_mov_b64_e32 v[140:141], 0
	v_mov_b64_e32 v[142:143], 0
	v_mov_b64_e32 v[144:145], 0
	v_mov_b64_e32 v[154:155], 0
	v_mov_b64_e32 v[156:157], 0
	v_mov_b64_e32 v[158:159], 0
	v_mov_b64_e32 v[160:161], 0
	s_bitcmp1_b32 s3, 2
	s_cbranch_scc1 .Lh1e_9967
	.p2align	6
.LBB0_372:
	ds_read_b128 v[18:21], v207
	ds_read_b128 v[22:25], v207 offset:1024
	ds_read_b128 v[26:29], v207 offset:2048
	ds_read_b128 v[30:33], v207 offset:3072
	ds_read_b128 v[2:5], v208
	ds_read_b128 v[6:9], v208 offset:1024
	ds_read_b128 v[10:13], v208 offset:2048
	ds_read_b128 v[14:17], v208 offset:3072
	s_add_u32 s28, s26, 0x8000
	s_addc_u32 s29, s27, 0
	s_cmp_eq_u32 s21, 12
	s_cselect_b32 s40, s22, s28
	s_cselect_b32 s41, s23, s29
	s_cselect_b32 s30, s24, s5
	s_cselect_b32 s31, s25, s19
	s_add_u32 s28, s40, 0x8000
	s_addc_u32 s29, s41, 0
	v_lshl_add_u64 v[244:245], s[26:27], 0, v[190:191]
	s_add_i32 m0, s46, 0xc000
	ds_read_b128 v[212:215], v209
	ds_read_b128 v[216:219], v209 offset:1024
	ds_read_b128 v[220:223], v209 offset:2048
	ds_read_b128 v[224:227], v209 offset:3072
	ds_read_b128 v[228:231], v209 offset:4096
	ds_read_b128 v[232:235], v209 offset:5120
	ds_read_b128 v[236:239], v209 offset:6144
	ds_read_b128 v[240:243], v209 offset:7168
	global_load_lds_dwordx4 v[244:245], off
	v_lshl_add_u64 v[244:245], s[26:27], 0, v[188:189]
	s_add_i32 m0, s46, 0xe000
	s_nop 0
	global_load_lds_dwordx4 v[244:245], off
	s_waitcnt vmcnt(8)
	s_waitcnt lgkmcnt(0)
	s_setprio 1
	v_mfma_scale_f32_16x16x128_f8f6f4 v[158:161], v[18:25], v[212:219], v[158:161], v210, v210 op_sel_hi:[0,0,0]
	v_mfma_scale_f32_16x16x128_f8f6f4 v[154:157], v[26:33], v[212:219], v[154:157], v210, v210 op_sel_hi:[0,0,0]
	v_mfma_scale_f32_16x16x128_f8f6f4 v[142:145], v[18:25], v[220:227], v[142:145], v210, v210 op_sel_hi:[0,0,0]
	v_mfma_scale_f32_16x16x128_f8f6f4 v[138:141], v[26:33], v[220:227], v[138:141], v210, v210 op_sel_hi:[0,0,0]
	v_mfma_scale_f32_16x16x128_f8f6f4 v[126:129], v[18:25], v[228:235], v[126:129], v210, v210 op_sel_hi:[0,0,0]
	v_mfma_scale_f32_16x16x128_f8f6f4 v[122:125], v[26:33], v[228:235], v[122:125], v210, v210 op_sel_hi:[0,0,0]
	v_mfma_scale_f32_16x16x128_f8f6f4 v[110:113], v[18:25], v[236:243], v[110:113], v210, v210 op_sel_hi:[0,0,0]
	v_mfma_scale_f32_16x16x128_f8f6f4 v[106:109], v[26:33], v[236:243], v[106:109], v210, v210 op_sel_hi:[0,0,0]
	s_nop 3
	s_setprio 0
	s_setprio 1
	v_mfma_scale_f32_16x16x128_f8f6f4 v[150:153], v[2:9], v[212:219], v[150:153], v210, v210 op_sel_hi:[0,0,0]
	v_mfma_scale_f32_16x16x128_f8f6f4 v[146:149], v[10:17], v[212:219], v[146:149], v210, v210 op_sel_hi:[0,0,0]
	v_mfma_scale_f32_16x16x128_f8f6f4 v[134:137], v[2:9], v[220:227], v[134:137], v210, v210 op_sel_hi:[0,0,0]
	v_mfma_scale_f32_16x16x128_f8f6f4 v[130:133], v[10:17], v[220:227], v[130:133], v210, v210 op_sel_hi:[0,0,0]
	v_mfma_scale_f32_16x16x128_f8f6f4 v[118:121], v[2:9], v[228:235], v[118:121], v210, v210 op_sel_hi:[0,0,0]
	v_mfma_scale_f32_16x16x128_f8f6f4 v[114:117], v[10:17], v[228:235], v[114:117], v210, v210 op_sel_hi:[0,0,0]
	v_mfma_scale_f32_16x16x128_f8f6f4 v[102:105], v[2:9], v[236:243], v[102:105], v210, v210 op_sel_hi:[0,0,0]
	v_mfma_scale_f32_16x16x128_f8f6f4 v[98:101], v[10:17], v[236:243], v[98:101], v210, v210 op_sel_hi:[0,0,0]
	s_setprio 0
	s_barrier
; #define PG8_STAGE(bufoff, gbase, voff) do { _Pragma("unroll") for (int _i = 0; _i < 2; ++_i) \
;         __builtin_amdgcn_global_load_lds((const unsigned*)((const char*)(gbase) + (voff)[_i]), (PG8_LAS unsigned*)(lds + (bufoff) + ldsw + _i * 8192), 16, 0, 0); } while (0)
; #define PG8_WAIT_V(n) asm volatile("s_waitcnt vmcnt(" #n ")" ::: "memory")
; #define PG8_WAIT_L(n) asm volatile("s_waitcnt lgkmcnt(" #n ")" ::: "memory")
; #define PG8_BAR __builtin_amdgcn_s_barrier()
; #define PG8_SCHED __builtin_amdgcn_sched_barrier(0)
; template <class Epi, class Sched, bool ALIGN_EPI = true, bool F8 = false>
; __device__ __forceinline__ void gemm_phase(PG8_LAS unsigned char* lds, const Sched& S, const Epi& E) {
;     ...
;             PG8_LDA(At, 0, 1); PG8_STAGE(PG8_SB(0, 0), b2, voffB[0]); PG8_STAGE(PG8_SB(0, 1), b2, voffB[1]); PG8_STAGE(PG8_SA(0, 0), a2, vA2[0]);
;             PG8_WAIT_V(8); PG8_WAIT_L(0); PG8_BAR; PG8_MMA(1, 0, At, B0); PG8_MMA(1, 1, At, B1); PG8_BAR; PG8_SCHED;
;             PG8_LDB(B0, 1, 0); PG8_LDB(B1, 1, 1); PG8_SCHED; PG8_LDA(At, 1, 0); PG8_STAGE(PG8_SA(0, 1), a2, vA2[1]);
;             PG8_WAIT_V(8); PG8_WAIT_L(0); PG8_BAR; PG8_MMA(0, 0, At, B0); PG8_MMA(0, 1, At, B1); PG8_BAR; PG8_SCHED;
	s_add_i32 s67, s62, s45
	v_lshl_add_u64 v[244:245], s[30:31], 0, v[164:165]
	s_mov_b32 m0, s67
	ds_read_b128 v[212:215], v209 offset:16384
	ds_read_b128 v[216:219], v209 offset:17408
	ds_read_b128 v[220:223], v209 offset:18432
	ds_read_b128 v[224:227], v209 offset:19456
	ds_read_b128 v[228:231], v209 offset:20480
	ds_read_b128 v[232:235], v209 offset:21504
	ds_read_b128 v[236:239], v209 offset:22528
	ds_read_b128 v[240:243], v209 offset:23552
	global_load_lds_dwordx4 v[244:245], off
	v_lshl_add_u64 v[246:247], s[30:31], 0, v[166:167]
	s_add_i32 m0, s67, 0x2000
	s_add_i32 s67, s63, s45
	global_load_lds_dwordx4 v[246:247], off
	v_lshl_add_u64 v[244:245], v[244:245], 0, s[8:9]
	s_mov_b32 m0, s67
	s_nop 0
	global_load_lds_dwordx4 v[244:245], off
	v_lshl_add_u64 v[244:245], v[246:247], 0, s[8:9]
	s_add_i32 m0, s67, 0x2000
	s_nop 0
	global_load_lds_dwordx4 v[244:245], off
	v_lshl_add_u64 v[244:245], s[40:41], 0, v[174:175]
	s_mov_b32 m0, s46
	s_nop 0
	global_load_lds_dwordx4 v[244:245], off
	v_lshl_add_u64 v[244:245], s[40:41], 0, v[176:177]
	s_mov_b32 m0, s47
	s_nop 0
	global_load_lds_dwordx4 v[244:245], off
	s_waitcnt vmcnt(8)
	s_waitcnt lgkmcnt(0)
	s_setprio 1
	v_mfma_scale_f32_16x16x128_f8f6f4 v[94:97], v[18:25], v[212:219], v[94:97], v210, v210 op_sel_hi:[0,0,0]
	v_mfma_scale_f32_16x16x128_f8f6f4 v[90:93], v[26:33], v[212:219], v[90:93], v210, v210 op_sel_hi:[0,0,0]
	v_mfma_scale_f32_16x16x128_f8f6f4 v[78:81], v[18:25], v[220:227], v[78:81], v210, v210 op_sel_hi:[0,0,0]
	v_mfma_scale_f32_16x16x128_f8f6f4 v[74:77], v[26:33], v[220:227], v[74:77], v210, v210 op_sel_hi:[0,0,0]
	v_mfma_scale_f32_16x16x128_f8f6f4 v[62:65], v[18:25], v[228:235], v[62:65], v210, v210 op_sel_hi:[0,0,0]
	v_mfma_scale_f32_16x16x128_f8f6f4 v[58:61], v[26:33], v[228:235], v[58:61], v210, v210 op_sel_hi:[0,0,0]
	v_mfma_scale_f32_16x16x128_f8f6f4 v[46:49], v[18:25], v[236:243], v[46:49], v210, v210 op_sel_hi:[0,0,0]
	v_mfma_scale_f32_16x16x128_f8f6f4 v[42:45], v[26:33], v[236:243], v[42:45], v210, v210 op_sel_hi:[0,0,0]
	s_nop 3
	s_setprio 0
	s_setprio 1
	v_mfma_scale_f32_16x16x128_f8f6f4 v[86:89], v[2:9], v[212:219], v[86:89], v210, v210 op_sel_hi:[0,0,0]
	v_mfma_scale_f32_16x16x128_f8f6f4 v[82:85], v[10:17], v[212:219], v[82:85], v210, v210 op_sel_hi:[0,0,0]
	v_mfma_scale_f32_16x16x128_f8f6f4 v[70:73], v[2:9], v[220:227], v[70:73], v210, v210 op_sel_hi:[0,0,0]
	v_mfma_scale_f32_16x16x128_f8f6f4 v[66:69], v[10:17], v[220:227], v[66:69], v210, v210 op_sel_hi:[0,0,0]
	v_mfma_scale_f32_16x16x128_f8f6f4 v[54:57], v[2:9], v[228:235], v[54:57], v210, v210 op_sel_hi:[0,0,0]
	v_mfma_scale_f32_16x16x128_f8f6f4 v[50:53], v[10:17], v[228:235], v[50:53], v210, v210 op_sel_hi:[0,0,0]
	v_mfma_scale_f32_16x16x128_f8f6f4 v[38:41], v[2:9], v[236:243], v[38:41], v210, v210 op_sel_hi:[0,0,0]
	v_mfma_scale_f32_16x16x128_f8f6f4 v[34:37], v[10:17], v[236:243], v[34:37], v210, v210 op_sel_hi:[0,0,0]
	s_setprio 0
	s_barrier
	s_add_i32 s67, 0, 0x18000
	s_add_i32 s68, 0, 0x1c000
	v_add_u32_e32 v14, s67, v202
	v_add_u32_e32 v30, s68, v202
	ds_read_b128 v[2:5], v14
	ds_read_b128 v[6:9], v14 offset:1024
	ds_read_b128 v[10:13], v14 offset:2048
	ds_read_b128 v[14:17], v14 offset:3072
	ds_read_b128 v[18:21], v30
	ds_read_b128 v[22:25], v30 offset:1024
	ds_read_b128 v[26:29], v30 offset:2048
	ds_read_b128 v[30:33], v30 offset:3072
	s_mov_b32 m0, s48
	v_lshl_add_u64 v[244:245], s[40:41], 0, v[178:179]
	ds_read_b128 v[212:215], v209 offset:32768
	ds_read_b128 v[216:219], v209 offset:33792
	ds_read_b128 v[220:223], v209 offset:34816
	ds_read_b128 v[224:227], v209 offset:35840
	ds_read_b128 v[228:231], v209 offset:36864
	ds_read_b128 v[232:235], v209 offset:37888
	ds_read_b128 v[236:239], v209 offset:38912
	ds_read_b128 v[240:243], v209 offset:39936
	global_load_lds_dwordx4 v[244:245], off
	v_lshl_add_u64 v[244:245], s[40:41], 0, v[180:181]
	s_mov_b32 m0, s49
	s_nop 0
	global_load_lds_dwordx4 v[244:245], off
	s_waitcnt vmcnt(8)
	s_waitcnt lgkmcnt(0)
	s_setprio 1
	v_mfma_scale_f32_16x16x128_f8f6f4 v[158:161], v[2:9], v[212:219], v[158:161], v210, v210 op_sel_hi:[0,0,0]
	v_mfma_scale_f32_16x16x128_f8f6f4 v[154:157], v[10:17], v[212:219], v[154:157], v210, v210 op_sel_hi:[0,0,0]
	v_mfma_scale_f32_16x16x128_f8f6f4 v[142:145], v[2:9], v[220:227], v[142:145], v210, v210 op_sel_hi:[0,0,0]
	v_mfma_scale_f32_16x16x128_f8f6f4 v[138:141], v[10:17], v[220:227], v[138:141], v210, v210 op_sel_hi:[0,0,0]
	v_mfma_scale_f32_16x16x128_f8f6f4 v[126:129], v[2:9], v[228:235], v[126:129], v210, v210 op_sel_hi:[0,0,0]
	v_mfma_scale_f32_16x16x128_f8f6f4 v[122:125], v[10:17], v[228:235], v[122:125], v210, v210 op_sel_hi:[0,0,0]
	v_mfma_scale_f32_16x16x128_f8f6f4 v[110:113], v[2:9], v[236:243], v[110:113], v210, v210 op_sel_hi:[0,0,0]
	v_mfma_scale_f32_16x16x128_f8f6f4 v[106:109], v[10:17], v[236:243], v[106:109], v210, v210 op_sel_hi:[0,0,0]
	s_nop 3
	s_setprio 0
	s_setprio 1
	v_mfma_scale_f32_16x16x128_f8f6f4 v[150:153], v[18:25], v[212:219], v[150:153], v210, v210 op_sel_hi:[0,0,0]
	v_mfma_scale_f32_16x16x128_f8f6f4 v[146:149], v[26:33], v[212:219], v[146:149], v210, v210 op_sel_hi:[0,0,0]
	v_mfma_scale_f32_16x16x128_f8f6f4 v[134:137], v[18:25], v[220:227], v[134:137], v210, v210 op_sel_hi:[0,0,0]
	v_mfma_scale_f32_16x16x128_f8f6f4 v[130:133], v[26:33], v[220:227], v[130:133], v210, v210 op_sel_hi:[0,0,0]
	v_mfma_scale_f32_16x16x128_f8f6f4 v[118:121], v[18:25], v[228:235], v[118:121], v210, v210 op_sel_hi:[0,0,0]
	v_mfma_scale_f32_16x16x128_f8f6f4 v[114:117], v[26:33], v[228:235], v[114:117], v210, v210 op_sel_hi:[0,0,0]
	v_mfma_scale_f32_16x16x128_f8f6f4 v[102:105], v[18:25], v[236:243], v[102:105], v210, v210 op_sel_hi:[0,0,0]
	v_mfma_scale_f32_16x16x128_f8f6f4 v[98:101], v[26:33], v[236:243], v[98:101], v210, v210 op_sel_hi:[0,0,0]
	s_setprio 0
	s_barrier
; #define PG8_STAGE(bufoff, gbase, voff) do { _Pragma("unroll") for (int _i = 0; _i < 2; ++_i) \
;         __builtin_amdgcn_global_load_lds((const unsigned*)((const char*)(gbase) + (voff)[_i]), (PG8_LAS unsigned*)(lds + (bufoff) + ldsw + _i * 8192), 16, 0, 0); } while (0)
; #define PG8_WAIT_V(n) asm volatile("s_waitcnt vmcnt(" #n ")" ::: "memory")
; #define PG8_WAIT_L(n) asm volatile("s_waitcnt lgkmcnt(" #n ")" ::: "memory")
; #define PG8_BAR __builtin_amdgcn_s_barrier()
; #define PG8_SCHED __builtin_amdgcn_sched_barrier(0)
; template <class Epi, class Sched, bool ALIGN_EPI = true, bool F8 = false>
; __device__ __forceinline__ void gemm_phase(PG8_LAS unsigned char* lds, const Sched& S, const Epi& E) {
;     ...
;             PG8_LDA(At, 1, 1); PG8_STAGE(PG8_SB(1, 0), b3, voffB[0]); PG8_STAGE(PG8_SB(1, 1), b3, voffB[1]); PG8_STAGE(PG8_SA(1, 0), a3, vA2[0]);
;             PG8_WAIT_V(8); PG8_WAIT_L(0); PG8_BAR; PG8_MMA(1, 0, At, B0); PG8_MMA(1, 1, At, B1); PG8_BAR; PG8_SCHED;
	s_add_u32 s30, s30, 0x8000
	s_addc_u32 s31, s31, 0
	s_add_i32 s40, s67, s45
	v_lshl_add_u64 v[244:245], s[30:31], 0, v[164:165]
	s_mov_b32 m0, s40
	ds_read_b128 v[212:215], v209 offset:49152
	ds_read_b128 v[216:219], v209 offset:50176
	ds_read_b128 v[220:223], v209 offset:51200
	ds_read_b128 v[224:227], v209 offset:52224
	ds_read_b128 v[228:231], v209 offset:53248
	ds_read_b128 v[232:235], v209 offset:54272
	ds_read_b128 v[236:239], v209 offset:55296
	ds_read_b128 v[240:243], v209 offset:56320
	global_load_lds_dwordx4 v[244:245], off
	v_lshl_add_u64 v[244:245], s[30:31], 0, v[166:167]
	s_add_i32 m0, s40, 0x2000
	s_add_i32 s40, s68, s45
	global_load_lds_dwordx4 v[244:245], off
	v_lshl_add_u64 v[244:245], s[30:31], 0, v[168:169]
	s_mov_b32 m0, s40
	s_nop 0
	global_load_lds_dwordx4 v[244:245], off
	v_lshl_add_u64 v[244:245], s[30:31], 0, v[172:173]
	s_add_i32 m0, s40, 0x2000
	s_nop 0
	global_load_lds_dwordx4 v[244:245], off
	v_lshl_add_u64 v[244:245], s[28:29], 0, v[174:175]
	s_mov_b32 m0, s52
	s_nop 0
	global_load_lds_dwordx4 v[244:245], off
	v_lshl_add_u64 v[244:245], s[28:29], 0, v[176:177]
	s_mov_b32 m0, s53
	s_nop 0
	global_load_lds_dwordx4 v[244:245], off
	s_waitcnt vmcnt(8)
	s_waitcnt lgkmcnt(0)
	s_setprio 1
	v_mfma_scale_f32_16x16x128_f8f6f4 v[94:97], v[2:9], v[212:219], v[94:97], v210, v210 op_sel_hi:[0,0,0]
	v_mfma_scale_f32_16x16x128_f8f6f4 v[90:93], v[10:17], v[212:219], v[90:93], v210, v210 op_sel_hi:[0,0,0]
	v_mfma_scale_f32_16x16x128_f8f6f4 v[78:81], v[2:9], v[220:227], v[78:81], v210, v210 op_sel_hi:[0,0,0]
	v_mfma_scale_f32_16x16x128_f8f6f4 v[74:77], v[10:17], v[220:227], v[74:77], v210, v210 op_sel_hi:[0,0,0]
	v_mfma_scale_f32_16x16x128_f8f6f4 v[62:65], v[2:9], v[228:235], v[62:65], v210, v210 op_sel_hi:[0,0,0]
	v_mfma_scale_f32_16x16x128_f8f6f4 v[58:61], v[10:17], v[228:235], v[58:61], v210, v210 op_sel_hi:[0,0,0]
	v_mfma_scale_f32_16x16x128_f8f6f4 v[46:49], v[2:9], v[236:243], v[46:49], v210, v210 op_sel_hi:[0,0,0]
	v_mfma_scale_f32_16x16x128_f8f6f4 v[42:45], v[10:17], v[236:243], v[42:45], v210, v210 op_sel_hi:[0,0,0]
	s_nop 3
	s_setprio 0
	s_setprio 1
	v_mfma_scale_f32_16x16x128_f8f6f4 v[86:89], v[18:25], v[212:219], v[86:89], v210, v210 op_sel_hi:[0,0,0]
	v_mfma_scale_f32_16x16x128_f8f6f4 v[82:85], v[26:33], v[212:219], v[82:85], v210, v210 op_sel_hi:[0,0,0]
	v_mfma_scale_f32_16x16x128_f8f6f4 v[70:73], v[18:25], v[220:227], v[70:73], v210, v210 op_sel_hi:[0,0,0]
	v_mfma_scale_f32_16x16x128_f8f6f4 v[66:69], v[26:33], v[220:227], v[66:69], v210, v210 op_sel_hi:[0,0,0]
	v_mfma_scale_f32_16x16x128_f8f6f4 v[54:57], v[18:25], v[228:235], v[54:57], v210, v210 op_sel_hi:[0,0,0]
	v_mfma_scale_f32_16x16x128_f8f6f4 v[50:53], v[26:33], v[228:235], v[50:53], v210, v210 op_sel_hi:[0,0,0]
	v_mfma_scale_f32_16x16x128_f8f6f4 v[38:41], v[18:25], v[236:243], v[38:41], v210, v210 op_sel_hi:[0,0,0]
	v_mfma_scale_f32_16x16x128_f8f6f4 v[34:37], v[26:33], v[236:243], v[34:37], v210, v210 op_sel_hi:[0,0,0]
	s_setprio 0
	s_barrier
	s_add_i32 s21, s21, 2
	s_add_u32 s5, s5, 0x10000
	s_addc_u32 s19, s19, 0
	s_add_u32 s26, s26, 0x10000
	s_addc_u32 s27, s27, 0
	s_cmp_gt_u32 s21, 13
	s_cbranch_scc0 .LBB0_372
	s_branch .Lfx_9967
	.p2align	6

; #define PG8_STAGE(bufoff, gbase, voff) do { _Pragma("unroll") for (int _i = 0; _i < 2; ++_i) \
;         __builtin_amdgcn_global_load_lds((const unsigned*)((const char*)(gbase) + (voff)[_i]), (PG8_LAS unsigned*)(lds + (bufoff) + ldsw + _i * 8192), 16, 0, 0); } while (0)
; #define PG8_WAIT_V(n) asm volatile("s_waitcnt vmcnt(" #n ")" ::: "memory")
; #define PG8_WAIT_L(n) asm volatile("s_waitcnt lgkmcnt(" #n ")" ::: "memory")
; #define PG8_BAR __builtin_amdgcn_s_barrier()
; #define PG8_SCHED __builtin_amdgcn_sched_barrier(0)
; template <class Epi, class Sched, bool ALIGN_EPI = true, bool F8 = false>
; __device__ __forceinline__ void gemm_phase(PG8_LAS unsigned char* lds, const Sched& S, const Epi& E) {
;     ...
;             PG8_LDB(B0, 0, 0); PG8_LDB(B1, 0, 1); PG8_SCHED; PG8_LDA(At, 0, 0); PG8_STAGE(PG8_SA(1, 1), a1, voffA[1]);
;             PG8_WAIT_V(8); PG8_WAIT_L(0); PG8_BAR; PG8_MMA(0, 0, At, B0); PG8_MMA(0, 1, At, B1); PG8_BAR; PG8_SCHED;
;             PG8_LDA(At, 0, 1); PG8_STAGE(PG8_SB(0, 0), b2, voffB[0]); PG8_STAGE(PG8_SB(0, 1), b2, voffB[1]); PG8_STAGE(PG8_SA(0, 0), a2, vA2[0]);
;             PG8_WAIT_V(8); PG8_WAIT_L(0); PG8_BAR; PG8_MMA(1, 0, At, B0); PG8_MMA(1, 1, At, B1); PG8_BAR; PG8_SCHED;
;     ...
; #pragma unroll
;         for (int a = 0; a < 2; ++a)
; #pragma unroll
;             for (int b = 0; b < 2; ++b)
; #pragma unroll
;                 for (int m = 0; m < 4; ++m)
; #pragma unroll
;                     for (int n = 0; n < 2; ++n) acc[a][b][m][n] = (f32x4){0.f, 0.f, 0.f, 0.f};
;         }
;         cur = nxt; cA = nA; cB = nB; ++ui;
; #pragma unroll
;         for (int h = 0; h < 2; ++h)
; #pragma unroll
;             for (int i = 0; i < 2; ++i) voffA[h][i] = voffAn[h][i];
.LBB0_427:
	s_add_u32 s17, s26, 0x10000
	s_addc_u32 s19, s27, 0
	s_add_u32 s24, s24, 0x8000
	v_mov_b64_e32 v[34:35], 0
	s_addc_u32 s25, s25, 0
	s_mov_b32 s74, -2
	v_mov_b64_e32 v[36:37], 0
	v_mov_b64_e32 v[38:39], 0
	v_mov_b64_e32 v[40:41], 0
	v_mov_b64_e32 v[50:51], 0
	v_mov_b64_e32 v[52:53], 0
	v_mov_b64_e32 v[54:55], 0
	v_mov_b64_e32 v[56:57], 0
	v_mov_b64_e32 v[66:67], 0
	v_mov_b64_e32 v[68:69], 0
	v_mov_b64_e32 v[70:71], 0
	v_mov_b64_e32 v[72:73], 0
	v_mov_b64_e32 v[82:83], 0
	v_mov_b64_e32 v[84:85], 0
	v_mov_b64_e32 v[86:87], 0
	v_mov_b64_e32 v[88:89], 0
	v_mov_b64_e32 v[42:43], 0
	v_mov_b64_e32 v[44:45], 0
	v_mov_b64_e32 v[46:47], 0
	v_mov_b64_e32 v[48:49], 0
	v_mov_b64_e32 v[58:59], 0
	v_mov_b64_e32 v[60:61], 0
	v_mov_b64_e32 v[62:63], 0
	v_mov_b64_e32 v[64:65], 0
	v_mov_b64_e32 v[74:75], 0
	v_mov_b64_e32 v[76:77], 0
	v_mov_b64_e32 v[78:79], 0
	v_mov_b64_e32 v[80:81], 0
	v_mov_b64_e32 v[90:91], 0
	v_mov_b64_e32 v[92:93], 0
	v_mov_b64_e32 v[94:95], 0
	v_mov_b64_e32 v[96:97], 0
	v_mov_b64_e32 v[98:99], 0
	v_mov_b64_e32 v[100:101], 0
	v_mov_b64_e32 v[102:103], 0
	v_mov_b64_e32 v[104:105], 0
	v_mov_b64_e32 v[114:115], 0
	v_mov_b64_e32 v[116:117], 0
	v_mov_b64_e32 v[118:119], 0
	v_mov_b64_e32 v[120:121], 0
	v_mov_b64_e32 v[130:131], 0
	v_mov_b64_e32 v[132:133], 0
	v_mov_b64_e32 v[134:135], 0
	v_mov_b64_e32 v[136:137], 0
	v_mov_b64_e32 v[146:147], 0
	v_mov_b64_e32 v[148:149], 0
	v_mov_b64_e32 v[150:151], 0
	v_mov_b64_e32 v[152:153], 0
	v_mov_b64_e32 v[106:107], 0
	v_mov_b64_e32 v[108:109], 0
	v_mov_b64_e32 v[110:111], 0
	v_mov_b64_e32 v[112:113], 0
	v_mov_b64_e32 v[122:123], 0
	v_mov_b64_e32 v[124:125], 0
	v_mov_b64_e32 v[126:127], 0
	v_mov_b64_e32 v[128:129], 0
	v_mov_b64_e32 v[138:139], 0
	v_mov_b64_e32 v[140:141], 0
	v_mov_b64_e32 v[142:143], 0
	v_mov_b64_e32 v[144:145], 0
	v_mov_b64_e32 v[154:155], 0
	v_mov_b64_e32 v[156:157], 0
	v_mov_b64_e32 v[158:159], 0
	v_mov_b64_e32 v[160:161], 0
	s_bitcmp1_b32 s3, 2
	s_cbranch_scc1 .Lh1e_11141
	.p2align	6
.LBB0_428:
	ds_read_b128 v[18:21], v192
	ds_read_b128 v[22:25], v192 offset:1024
	ds_read_b128 v[26:29], v192 offset:2048
	ds_read_b128 v[30:33], v192 offset:3072
	ds_read_b128 v[2:5], v193
	ds_read_b128 v[6:9], v193 offset:1024
	ds_read_b128 v[10:13], v193 offset:2048
	ds_read_b128 v[14:17], v193 offset:3072
	s_add_u32 s26, s24, 0x8000
	s_addc_u32 s27, s25, 0
	s_cmp_eq_u32 s74, 12
	s_cselect_b32 s30, s20, s26
	s_cselect_b32 s31, s21, s27
	s_cselect_b32 s28, s22, s17
	s_cselect_b32 s29, s23, s19
	s_add_u32 s26, s30, 0x8000
	s_addc_u32 s27, s31, 0
	v_lshl_add_u64 v[230:231], s[24:25], 0, v[184:185]
	s_add_i32 m0, s48, 0xc000
	ds_read_b128 v[198:201], v194
	ds_read_b128 v[202:205], v194 offset:1024
	ds_read_b128 v[206:209], v194 offset:2048
	ds_read_b128 v[210:213], v194 offset:3072
	ds_read_b128 v[214:217], v194 offset:4096
	ds_read_b128 v[218:221], v194 offset:5120
	ds_read_b128 v[222:225], v194 offset:6144
	ds_read_b128 v[226:229], v194 offset:7168
	global_load_lds_dwordx4 v[230:231], off
	v_lshl_add_u64 v[230:231], s[24:25], 0, v[182:183]
	s_add_i32 m0, s48, 0xe000
	s_nop 0
	global_load_lds_dwordx4 v[230:231], off
	s_waitcnt vmcnt(8)
	s_waitcnt lgkmcnt(0)
	s_setprio 1
	v_mfma_scale_f32_16x16x128_f8f6f4 v[158:161], v[18:25], v[198:205], v[158:161], v195, v195 op_sel_hi:[0,0,0]
	v_mfma_scale_f32_16x16x128_f8f6f4 v[154:157], v[26:33], v[198:205], v[154:157], v195, v195 op_sel_hi:[0,0,0]
	v_mfma_scale_f32_16x16x128_f8f6f4 v[142:145], v[18:25], v[206:213], v[142:145], v195, v195 op_sel_hi:[0,0,0]
	v_mfma_scale_f32_16x16x128_f8f6f4 v[138:141], v[26:33], v[206:213], v[138:141], v195, v195 op_sel_hi:[0,0,0]
	v_mfma_scale_f32_16x16x128_f8f6f4 v[126:129], v[18:25], v[214:221], v[126:129], v195, v195 op_sel_hi:[0,0,0]
	v_mfma_scale_f32_16x16x128_f8f6f4 v[122:125], v[26:33], v[214:221], v[122:125], v195, v195 op_sel_hi:[0,0,0]
	v_mfma_scale_f32_16x16x128_f8f6f4 v[110:113], v[18:25], v[222:229], v[110:113], v195, v195 op_sel_hi:[0,0,0]
	v_mfma_scale_f32_16x16x128_f8f6f4 v[106:109], v[26:33], v[222:229], v[106:109], v195, v195 op_sel_hi:[0,0,0]
	s_nop 3
	s_setprio 0
	s_setprio 1
	v_mfma_scale_f32_16x16x128_f8f6f4 v[150:153], v[2:9], v[198:205], v[150:153], v195, v195 op_sel_hi:[0,0,0]
	v_mfma_scale_f32_16x16x128_f8f6f4 v[146:149], v[10:17], v[198:205], v[146:149], v195, v195 op_sel_hi:[0,0,0]
	v_mfma_scale_f32_16x16x128_f8f6f4 v[134:137], v[2:9], v[206:213], v[134:137], v195, v195 op_sel_hi:[0,0,0]
	v_mfma_scale_f32_16x16x128_f8f6f4 v[130:133], v[10:17], v[206:213], v[130:133], v195, v195 op_sel_hi:[0,0,0]
	v_mfma_scale_f32_16x16x128_f8f6f4 v[118:121], v[2:9], v[214:221], v[118:121], v195, v195 op_sel_hi:[0,0,0]
	v_mfma_scale_f32_16x16x128_f8f6f4 v[114:117], v[10:17], v[214:221], v[114:117], v195, v195 op_sel_hi:[0,0,0]
	v_mfma_scale_f32_16x16x128_f8f6f4 v[102:105], v[2:9], v[222:229], v[102:105], v195, v195 op_sel_hi:[0,0,0]
	v_mfma_scale_f32_16x16x128_f8f6f4 v[98:101], v[10:17], v[222:229], v[98:101], v195, v195 op_sel_hi:[0,0,0]
	s_setprio 0
	s_barrier
; #define PG8_STAGE(bufoff, gbase, voff) do { _Pragma("unroll") for (int _i = 0; _i < 2; ++_i) \
;         __builtin_amdgcn_global_load_lds((const unsigned*)((const char*)(gbase) + (voff)[_i]), (PG8_LAS unsigned*)(lds + (bufoff) + ldsw + _i * 8192), 16, 0, 0); } while (0)
; #define PG8_WAIT_V(n) asm volatile("s_waitcnt vmcnt(" #n ")" ::: "memory")
; #define PG8_WAIT_L(n) asm volatile("s_waitcnt lgkmcnt(" #n ")" ::: "memory")
; #define PG8_BAR __builtin_amdgcn_s_barrier()
; #define PG8_SCHED __builtin_amdgcn_sched_barrier(0)
; template <class Epi, class Sched, bool ALIGN_EPI = true, bool F8 = false>
; __device__ __forceinline__ void gemm_phase(PG8_LAS unsigned char* lds, const Sched& S, const Epi& E) {
;     ...
;             PG8_LDA(At, 0, 1); PG8_STAGE(PG8_SB(0, 0), b2, voffB[0]); PG8_STAGE(PG8_SB(0, 1), b2, voffB[1]); PG8_STAGE(PG8_SA(0, 0), a2, vA2[0]);
;             PG8_WAIT_V(8); PG8_WAIT_L(0); PG8_BAR; PG8_MMA(1, 0, At, B0); PG8_MMA(1, 1, At, B1); PG8_BAR; PG8_SCHED;
;             PG8_LDB(B0, 1, 0); PG8_LDB(B1, 1, 1); PG8_SCHED; PG8_LDA(At, 1, 0); PG8_STAGE(PG8_SA(0, 1), a2, vA2[1]);
;             PG8_WAIT_V(8); PG8_WAIT_L(0); PG8_BAR; PG8_MMA(0, 0, At, B0); PG8_MMA(0, 1, At, B1); PG8_BAR; PG8_SCHED;
	s_add_i32 s75, s65, s47
	v_lshl_add_u64 v[230:231], s[28:29], 0, v[164:165]
	s_mov_b32 m0, s75
	ds_read_b128 v[198:201], v194 offset:16384
	ds_read_b128 v[202:205], v194 offset:17408
	ds_read_b128 v[206:209], v194 offset:18432
	ds_read_b128 v[210:213], v194 offset:19456
	ds_read_b128 v[214:217], v194 offset:20480
	ds_read_b128 v[218:221], v194 offset:21504
	ds_read_b128 v[222:225], v194 offset:22528
	ds_read_b128 v[226:229], v194 offset:23552
	global_load_lds_dwordx4 v[230:231], off
	v_lshl_add_u64 v[232:233], s[28:29], 0, v[166:167]
	s_add_i32 m0, s75, 0x2000
	s_add_i32 s75, s66, s47
	global_load_lds_dwordx4 v[232:233], off
	v_lshl_add_u64 v[230:231], v[230:231], 0, s[4:5]
	s_mov_b32 m0, s75
	s_nop 0
	global_load_lds_dwordx4 v[230:231], off
	v_lshl_add_u64 v[230:231], v[232:233], 0, s[4:5]
	s_add_i32 m0, s75, 0x2000
	s_nop 0
	global_load_lds_dwordx4 v[230:231], off
	v_lshl_add_u64 v[230:231], s[30:31], 0, v[174:175]
	s_mov_b32 m0, s48
	s_nop 0
	global_load_lds_dwordx4 v[230:231], off
	v_lshl_add_u64 v[230:231], s[30:31], 0, v[176:177]
	s_mov_b32 m0, s49
	s_nop 0
	global_load_lds_dwordx4 v[230:231], off
	s_waitcnt vmcnt(8)
	s_waitcnt lgkmcnt(0)
	s_setprio 1
	v_mfma_scale_f32_16x16x128_f8f6f4 v[94:97], v[18:25], v[198:205], v[94:97], v195, v195 op_sel_hi:[0,0,0]
	v_mfma_scale_f32_16x16x128_f8f6f4 v[90:93], v[26:33], v[198:205], v[90:93], v195, v195 op_sel_hi:[0,0,0]
	v_mfma_scale_f32_16x16x128_f8f6f4 v[78:81], v[18:25], v[206:213], v[78:81], v195, v195 op_sel_hi:[0,0,0]
	v_mfma_scale_f32_16x16x128_f8f6f4 v[74:77], v[26:33], v[206:213], v[74:77], v195, v195 op_sel_hi:[0,0,0]
	v_mfma_scale_f32_16x16x128_f8f6f4 v[62:65], v[18:25], v[214:221], v[62:65], v195, v195 op_sel_hi:[0,0,0]
	v_mfma_scale_f32_16x16x128_f8f6f4 v[58:61], v[26:33], v[214:221], v[58:61], v195, v195 op_sel_hi:[0,0,0]
	v_mfma_scale_f32_16x16x128_f8f6f4 v[46:49], v[18:25], v[222:229], v[46:49], v195, v195 op_sel_hi:[0,0,0]
	v_mfma_scale_f32_16x16x128_f8f6f4 v[42:45], v[26:33], v[222:229], v[42:45], v195, v195 op_sel_hi:[0,0,0]
	s_nop 3
	s_setprio 0
	s_setprio 1
	v_mfma_scale_f32_16x16x128_f8f6f4 v[86:89], v[2:9], v[198:205], v[86:89], v195, v195 op_sel_hi:[0,0,0]
	v_mfma_scale_f32_16x16x128_f8f6f4 v[82:85], v[10:17], v[198:205], v[82:85], v195, v195 op_sel_hi:[0,0,0]
	v_mfma_scale_f32_16x16x128_f8f6f4 v[70:73], v[2:9], v[206:213], v[70:73], v195, v195 op_sel_hi:[0,0,0]
	v_mfma_scale_f32_16x16x128_f8f6f4 v[66:69], v[10:17], v[206:213], v[66:69], v195, v195 op_sel_hi:[0,0,0]
	v_mfma_scale_f32_16x16x128_f8f6f4 v[54:57], v[2:9], v[214:221], v[54:57], v195, v195 op_sel_hi:[0,0,0]
	v_mfma_scale_f32_16x16x128_f8f6f4 v[50:53], v[10:17], v[214:221], v[50:53], v195, v195 op_sel_hi:[0,0,0]
	v_mfma_scale_f32_16x16x128_f8f6f4 v[38:41], v[2:9], v[222:229], v[38:41], v195, v195 op_sel_hi:[0,0,0]
	v_mfma_scale_f32_16x16x128_f8f6f4 v[34:37], v[10:17], v[222:229], v[34:37], v195, v195 op_sel_hi:[0,0,0]
	s_setprio 0
	s_barrier
	s_add_i32 s75, 0, 0x18000
	s_add_i32 s76, 0, 0x1c000
	v_add_u32_e32 v14, s75, v191
	v_add_u32_e32 v30, s76, v191
	ds_read_b128 v[2:5], v14
	ds_read_b128 v[6:9], v14 offset:1024
	ds_read_b128 v[10:13], v14 offset:2048
	ds_read_b128 v[14:17], v14 offset:3072
	ds_read_b128 v[18:21], v30
	ds_read_b128 v[22:25], v30 offset:1024
	ds_read_b128 v[26:29], v30 offset:2048
	ds_read_b128 v[30:33], v30 offset:3072
	s_mov_b32 m0, s50
	v_lshl_add_u64 v[230:231], s[30:31], 0, v[178:179]
	ds_read_b128 v[198:201], v194 offset:32768
	ds_read_b128 v[202:205], v194 offset:33792
	ds_read_b128 v[206:209], v194 offset:34816
	ds_read_b128 v[210:213], v194 offset:35840
	ds_read_b128 v[214:217], v194 offset:36864
	ds_read_b128 v[218:221], v194 offset:37888
	ds_read_b128 v[222:225], v194 offset:38912
	ds_read_b128 v[226:229], v194 offset:39936
	global_load_lds_dwordx4 v[230:231], off
	v_lshl_add_u64 v[230:231], s[30:31], 0, v[180:181]
	s_mov_b32 m0, s51
	s_nop 0
	global_load_lds_dwordx4 v[230:231], off
	s_waitcnt vmcnt(8)
	s_waitcnt lgkmcnt(0)
	s_setprio 1
	v_mfma_scale_f32_16x16x128_f8f6f4 v[158:161], v[2:9], v[198:205], v[158:161], v195, v195 op_sel_hi:[0,0,0]
	v_mfma_scale_f32_16x16x128_f8f6f4 v[154:157], v[10:17], v[198:205], v[154:157], v195, v195 op_sel_hi:[0,0,0]
	v_mfma_scale_f32_16x16x128_f8f6f4 v[142:145], v[2:9], v[206:213], v[142:145], v195, v195 op_sel_hi:[0,0,0]
	v_mfma_scale_f32_16x16x128_f8f6f4 v[138:141], v[10:17], v[206:213], v[138:141], v195, v195 op_sel_hi:[0,0,0]
	v_mfma_scale_f32_16x16x128_f8f6f4 v[126:129], v[2:9], v[214:221], v[126:129], v195, v195 op_sel_hi:[0,0,0]
	v_mfma_scale_f32_16x16x128_f8f6f4 v[122:125], v[10:17], v[214:221], v[122:125], v195, v195 op_sel_hi:[0,0,0]
	v_mfma_scale_f32_16x16x128_f8f6f4 v[110:113], v[2:9], v[222:229], v[110:113], v195, v195 op_sel_hi:[0,0,0]
	v_mfma_scale_f32_16x16x128_f8f6f4 v[106:109], v[10:17], v[222:229], v[106:109], v195, v195 op_sel_hi:[0,0,0]
	s_nop 3
	s_setprio 0
	s_setprio 1
	v_mfma_scale_f32_16x16x128_f8f6f4 v[150:153], v[18:25], v[198:205], v[150:153], v195, v195 op_sel_hi:[0,0,0]
	v_mfma_scale_f32_16x16x128_f8f6f4 v[146:149], v[26:33], v[198:205], v[146:149], v195, v195 op_sel_hi:[0,0,0]
	v_mfma_scale_f32_16x16x128_f8f6f4 v[134:137], v[18:25], v[206:213], v[134:137], v195, v195 op_sel_hi:[0,0,0]
	v_mfma_scale_f32_16x16x128_f8f6f4 v[130:133], v[26:33], v[206:213], v[130:133], v195, v195 op_sel_hi:[0,0,0]
	v_mfma_scale_f32_16x16x128_f8f6f4 v[118:121], v[18:25], v[214:221], v[118:121], v195, v195 op_sel_hi:[0,0,0]
	v_mfma_scale_f32_16x16x128_f8f6f4 v[114:117], v[26:33], v[214:221], v[114:117], v195, v195 op_sel_hi:[0,0,0]
	v_mfma_scale_f32_16x16x128_f8f6f4 v[102:105], v[18:25], v[222:229], v[102:105], v195, v195 op_sel_hi:[0,0,0]
	v_mfma_scale_f32_16x16x128_f8f6f4 v[98:101], v[26:33], v[222:229], v[98:101], v195, v195 op_sel_hi:[0,0,0]
	s_setprio 0
	s_barrier
; #define PG8_STAGE(bufoff, gbase, voff) do { _Pragma("unroll") for (int _i = 0; _i < 2; ++_i) \
;         __builtin_amdgcn_global_load_lds((const unsigned*)((const char*)(gbase) + (voff)[_i]), (PG8_LAS unsigned*)(lds + (bufoff) + ldsw + _i * 8192), 16, 0, 0); } while (0)
; #define PG8_WAIT_V(n) asm volatile("s_waitcnt vmcnt(" #n ")" ::: "memory")
; #define PG8_WAIT_L(n) asm volatile("s_waitcnt lgkmcnt(" #n ")" ::: "memory")
; #define PG8_BAR __builtin_amdgcn_s_barrier()
; #define PG8_SCHED __builtin_amdgcn_sched_barrier(0)
; template <class Epi, class Sched, bool ALIGN_EPI = true, bool F8 = false>
; __device__ __forceinline__ void gemm_phase(PG8_LAS unsigned char* lds, const Sched& S, const Epi& E) {
;     ...
;             PG8_LDA(At, 1, 1); PG8_STAGE(PG8_SB(1, 0), b3, voffB[0]); PG8_STAGE(PG8_SB(1, 1), b3, voffB[1]); PG8_STAGE(PG8_SA(1, 0), a3, vA2[0]);
;             PG8_WAIT_V(8); PG8_WAIT_L(0); PG8_BAR; PG8_MMA(1, 0, At, B0); PG8_MMA(1, 1, At, B1); PG8_BAR; PG8_SCHED;
	s_add_u32 s28, s28, 0x8000
	s_addc_u32 s29, s29, 0
	s_add_i32 s30, s75, s47
	v_lshl_add_u64 v[230:231], s[28:29], 0, v[164:165]
	s_mov_b32 m0, s30
	ds_read_b128 v[198:201], v194 offset:49152
	ds_read_b128 v[202:205], v194 offset:50176
	ds_read_b128 v[206:209], v194 offset:51200
	ds_read_b128 v[210:213], v194 offset:52224
	ds_read_b128 v[214:217], v194 offset:53248
	ds_read_b128 v[218:221], v194 offset:54272
	ds_read_b128 v[222:225], v194 offset:55296
	ds_read_b128 v[226:229], v194 offset:56320
	global_load_lds_dwordx4 v[230:231], off
	v_lshl_add_u64 v[230:231], s[28:29], 0, v[166:167]
	s_add_i32 m0, s30, 0x2000
	s_add_i32 s30, s76, s47
	global_load_lds_dwordx4 v[230:231], off
	v_lshl_add_u64 v[230:231], s[28:29], 0, v[168:169]
	s_mov_b32 m0, s30
	s_nop 0
	global_load_lds_dwordx4 v[230:231], off
	v_lshl_add_u64 v[230:231], s[28:29], 0, v[172:173]
	s_add_i32 m0, s30, 0x2000
	s_nop 0
	global_load_lds_dwordx4 v[230:231], off
	v_lshl_add_u64 v[230:231], s[26:27], 0, v[174:175]
	s_mov_b32 m0, s60
	s_nop 0
	global_load_lds_dwordx4 v[230:231], off
	v_lshl_add_u64 v[230:231], s[26:27], 0, v[176:177]
	s_mov_b32 m0, s61
	s_nop 0
	global_load_lds_dwordx4 v[230:231], off
	s_waitcnt vmcnt(8)
	s_waitcnt lgkmcnt(0)
	s_setprio 1
	v_mfma_scale_f32_16x16x128_f8f6f4 v[94:97], v[2:9], v[198:205], v[94:97], v195, v195 op_sel_hi:[0,0,0]
	v_mfma_scale_f32_16x16x128_f8f6f4 v[90:93], v[10:17], v[198:205], v[90:93], v195, v195 op_sel_hi:[0,0,0]
	v_mfma_scale_f32_16x16x128_f8f6f4 v[78:81], v[2:9], v[206:213], v[78:81], v195, v195 op_sel_hi:[0,0,0]
	v_mfma_scale_f32_16x16x128_f8f6f4 v[74:77], v[10:17], v[206:213], v[74:77], v195, v195 op_sel_hi:[0,0,0]
	v_mfma_scale_f32_16x16x128_f8f6f4 v[62:65], v[2:9], v[214:221], v[62:65], v195, v195 op_sel_hi:[0,0,0]
	v_mfma_scale_f32_16x16x128_f8f6f4 v[58:61], v[10:17], v[214:221], v[58:61], v195, v195 op_sel_hi:[0,0,0]
	v_mfma_scale_f32_16x16x128_f8f6f4 v[46:49], v[2:9], v[222:229], v[46:49], v195, v195 op_sel_hi:[0,0,0]
	v_mfma_scale_f32_16x16x128_f8f6f4 v[42:45], v[10:17], v[222:229], v[42:45], v195, v195 op_sel_hi:[0,0,0]
	s_nop 3
	s_setprio 0
	s_setprio 1
	v_mfma_scale_f32_16x16x128_f8f6f4 v[86:89], v[18:25], v[198:205], v[86:89], v195, v195 op_sel_hi:[0,0,0]
	v_mfma_scale_f32_16x16x128_f8f6f4 v[82:85], v[26:33], v[198:205], v[82:85], v195, v195 op_sel_hi:[0,0,0]
	v_mfma_scale_f32_16x16x128_f8f6f4 v[70:73], v[18:25], v[206:213], v[70:73], v195, v195 op_sel_hi:[0,0,0]
	v_mfma_scale_f32_16x16x128_f8f6f4 v[66:69], v[26:33], v[206:213], v[66:69], v195, v195 op_sel_hi:[0,0,0]
	v_mfma_scale_f32_16x16x128_f8f6f4 v[54:57], v[18:25], v[214:221], v[54:57], v195, v195 op_sel_hi:[0,0,0]
	v_mfma_scale_f32_16x16x128_f8f6f4 v[50:53], v[26:33], v[214:221], v[50:53], v195, v195 op_sel_hi:[0,0,0]
	v_mfma_scale_f32_16x16x128_f8f6f4 v[38:41], v[18:25], v[222:229], v[38:41], v195, v195 op_sel_hi:[0,0,0]
	v_mfma_scale_f32_16x16x128_f8f6f4 v[34:37], v[26:33], v[222:229], v[34:37], v195, v195 op_sel_hi:[0,0,0]
	s_setprio 0
	s_barrier
	s_add_i32 s74, s74, 2
	s_add_u32 s17, s17, 0x10000
	s_addc_u32 s19, s19, 0
	s_add_u32 s24, s24, 0x10000
	s_addc_u32 s25, s25, 0
	s_cmp_gt_u32 s74, 13
	s_cbranch_scc0 .LBB0_428
	s_branch .Lfx_11141
	.p2align	6

; #define PG8_STAGE(bufoff, gbase, voff) do { _Pragma("unroll") for (int _i = 0; _i < 2; ++_i) \
;         __builtin_amdgcn_global_load_lds((const unsigned*)((const char*)(gbase) + (voff)[_i]), (PG8_LAS unsigned*)(lds + (bufoff) + ldsw + _i * 8192), 16, 0, 0); } while (0)
; #define PG8_WAIT_V(n) asm volatile("s_waitcnt vmcnt(" #n ")" ::: "memory")
; #define PG8_WAIT_L(n) asm volatile("s_waitcnt lgkmcnt(" #n ")" ::: "memory")
; #define PG8_BAR __builtin_amdgcn_s_barrier()
; #define PG8_SCHED __builtin_amdgcn_sched_barrier(0)
; template <class Epi, class Sched, bool ALIGN_EPI = true, bool F8 = false>
; __device__ __forceinline__ void gemm_phase(PG8_LAS unsigned char* lds, const Sched& S, const Epi& E) {
;     ...
;         for (int t = 0; t < nt; t += 2) {
;             const bool last = (t == nt - 2);
;             if constexpr (Sched::GATHER) { if (last && has_next) S.a_off(nxt, Rs, Cs, voffAn); }
;             const char* a1 = cA + (size_t)(t + 1) * kstep;
;             const char* a2 = last ? nA : cA + (size_t)(t + 2) * kstep; const char* b2 = last ? nB : cB + (size_t)(t + 2) * kstepB;
;             const char* a3 = a2 + kstep; const char* b3 = b2 + kstepB;
;             unsigned vA2[2][2];
; #pragma unroll
;             for (int h = 0; h < 2; ++h)
; #pragma unroll
;                 for (int i = 0; i < 2; ++i) { if constexpr (Sched::GATHER) vA2[h][i] = (last && has_next) ? voffAn[h][i] : voffA[h][i]; else vA2[h][i] = voffA[h][i]; }
;             PG8_LDB(B0, 0, 0); PG8_LDB(B1, 0, 1); PG8_SCHED; PG8_LDA(At, 0, 0); PG8_STAGE(PG8_SA(1, 1), a1, voffA[1]);
;             PG8_WAIT_V(8); PG8_WAIT_L(0); PG8_BAR; PG8_MMA(0, 0, At, B0); PG8_MMA(0, 1, At, B1); PG8_BAR; PG8_SCHED;
;             PG8_LDA(At, 0, 1); PG8_STAGE(PG8_SB(0, 0), b2, voffB[0]); PG8_STAGE(PG8_SB(0, 1), b2, voffB[1]); PG8_STAGE(PG8_SA(0, 0), a2, vA2[0]);
;             PG8_WAIT_V(8); PG8_WAIT_L(0); PG8_BAR; PG8_MMA(1, 0, At, B0); PG8_MMA(1, 1, At, B1); PG8_BAR; PG8_SCHED;
;             PG8_LDB(B0, 1, 0); PG8_LDB(B1, 1, 1); PG8_SCHED; PG8_LDA(At, 1, 0); PG8_STAGE(PG8_SA(0, 1), a2, vA2[1]);
;             PG8_WAIT_V(8); PG8_WAIT_L(0); PG8_BAR; PG8_MMA(0, 0, At, B0); PG8_MMA(0, 1, At, B1); PG8_BAR; PG8_SCHED;
.LBB0_833:
	s_add_i32 s74, s72, -2
	s_add_u32 s75, s26, 0x10000
	s_addc_u32 s76, s27, 0
	s_add_u32 s24, s24, 0x8000
	s_addc_u32 s25, s25, 0
	s_mov_b32 s26, 0
	s_bitcmp1_b32 s3, 2
	s_cbranch_scc1 .Lh1e_23459
	.p2align	6
.LBB0_834:
	v_add_u32_e32 v10, s58, v190
	ds_read_b128 v[2:5], v10
	ds_read_b128 v[6:9], v10 offset:1024
	ds_read_b128 v[142:145], v10 offset:2048
	ds_read_b128 v[146:149], v10 offset:3072
	v_add_u32_e32 v10, s59, v190
	ds_read_b128 v[150:153], v10
	ds_read_b128 v[154:157], v10 offset:1024
	ds_read_b128 v[202:205], v10 offset:2048
	ds_read_b128 v[206:209], v10 offset:3072
	s_add_i32 s77, s26, 2
	s_add_u32 s27, s24, 0x8000
	s_addc_u32 s28, s25, 0
	s_cmp_eq_u32 s74, s26
	s_cselect_b32 s30, s20, s27
	s_cselect_b32 s31, s21, s28
	s_cselect_b32 s28, s22, s75
	s_cselect_b32 s29, s23, s76
	s_add_u32 s26, s30, 0x8000
	s_addc_u32 s27, s31, 0
	v_lshl_add_u64 v[12:13], s[24:25], 0, v[182:183]
	s_add_i32 m0, s45, 0xc000
	ds_read_b128 v[210:213], v198
	ds_read_b128 v[214:217], v198 offset:1024
	ds_read_b128 v[218:221], v198 offset:2048
	ds_read_b128 v[222:225], v198 offset:3072
	ds_read_b128 v[226:229], v198 offset:4096
	ds_read_b128 v[230:233], v198 offset:5120
	ds_read_b128 v[234:237], v198 offset:6144
	ds_read_b128 v[238:241], v198 offset:7168
	global_load_lds_dwordx4 v[12:13], off
	v_lshl_add_u64 v[12:13], s[24:25], 0, v[180:181]
	s_add_i32 m0, s45, 0xe000
	s_nop 0
	global_load_lds_dwordx4 v[12:13], off
	s_waitcnt vmcnt(8)
	s_waitcnt lgkmcnt(0)
	s_setprio 1
	v_mfma_scale_f32_16x16x128_f8f6f4 v[138:141], v[2:9], v[210:217], v[138:141], v199, v199 op_sel_hi:[0,0,0]
	v_mfma_scale_f32_16x16x128_f8f6f4 v[134:137], v[142:149], v[210:217], v[134:137], v199, v199 op_sel_hi:[0,0,0]
	v_mfma_scale_f32_16x16x128_f8f6f4 v[130:133], v[2:9], v[218:225], v[130:133], v199, v199 op_sel_hi:[0,0,0]
	v_mfma_scale_f32_16x16x128_f8f6f4 v[126:129], v[142:149], v[218:225], v[126:129], v199, v199 op_sel_hi:[0,0,0]
	v_mfma_scale_f32_16x16x128_f8f6f4 v[122:125], v[2:9], v[226:233], v[122:125], v199, v199 op_sel_hi:[0,0,0]
	v_mfma_scale_f32_16x16x128_f8f6f4 v[118:121], v[142:149], v[226:233], v[118:121], v199, v199 op_sel_hi:[0,0,0]
	v_mfma_scale_f32_16x16x128_f8f6f4 v[114:117], v[2:9], v[234:241], v[114:117], v199, v199 op_sel_hi:[0,0,0]
	v_mfma_scale_f32_16x16x128_f8f6f4 v[110:113], v[142:149], v[234:241], v[110:113], v199, v199 op_sel_hi:[0,0,0]
	s_nop 3
	s_setprio 0
	s_setprio 1
	v_mfma_scale_f32_16x16x128_f8f6f4 v[106:109], v[150:157], v[210:217], v[106:109], v199, v199 op_sel_hi:[0,0,0]
	v_mfma_scale_f32_16x16x128_f8f6f4 v[102:105], v[202:209], v[210:217], v[102:105], v199, v199 op_sel_hi:[0,0,0]
	v_mfma_scale_f32_16x16x128_f8f6f4 v[98:101], v[150:157], v[218:225], v[98:101], v199, v199 op_sel_hi:[0,0,0]
	v_mfma_scale_f32_16x16x128_f8f6f4 v[94:97], v[202:209], v[218:225], v[94:97], v199, v199 op_sel_hi:[0,0,0]
	v_mfma_scale_f32_16x16x128_f8f6f4 v[90:93], v[150:157], v[226:233], v[90:93], v199, v199 op_sel_hi:[0,0,0]
	v_mfma_scale_f32_16x16x128_f8f6f4 v[86:89], v[202:209], v[226:233], v[86:89], v199, v199 op_sel_hi:[0,0,0]
	v_mfma_scale_f32_16x16x128_f8f6f4 v[82:85], v[150:157], v[234:241], v[82:85], v199, v199 op_sel_hi:[0,0,0]
	v_mfma_scale_f32_16x16x128_f8f6f4 v[78:81], v[202:209], v[234:241], v[78:81], v199, v199 op_sel_hi:[0,0,0]
	s_setprio 0
	s_barrier
	s_add_i32 s78, s58, s44
	v_lshl_add_u64 v[12:13], s[28:29], 0, v[158:159]
	s_mov_b32 m0, s78
	ds_read_b128 v[210:213], v198 offset:16384
	ds_read_b128 v[214:217], v198 offset:17408
	ds_read_b128 v[218:221], v198 offset:18432
	ds_read_b128 v[222:225], v198 offset:19456
	ds_read_b128 v[226:229], v198 offset:20480
	ds_read_b128 v[230:233], v198 offset:21504
	ds_read_b128 v[234:237], v198 offset:22528
	ds_read_b128 v[238:241], v198 offset:23552
	global_load_lds_dwordx4 v[12:13], off
	v_lshl_add_u64 v[188:189], s[28:29], 0, v[160:161]
	s_add_i32 m0, s78, 0x2000
	s_add_i32 s78, s59, s44
	global_load_lds_dwordx4 v[188:189], off
	v_lshl_add_u64 v[12:13], v[12:13], 0, s[8:9]
	s_mov_b32 m0, s78
	s_nop 0
	global_load_lds_dwordx4 v[12:13], off
	v_lshl_add_u64 v[12:13], v[188:189], 0, s[8:9]
	s_add_i32 m0, s78, 0x2000
	s_nop 0
	global_load_lds_dwordx4 v[12:13], off
	v_lshl_add_u64 v[12:13], s[30:31], 0, v[162:163]
	s_mov_b32 m0, s45
	s_nop 0
	global_load_lds_dwordx4 v[12:13], off
	v_lshl_add_u64 v[12:13], s[30:31], 0, v[164:165]
	s_mov_b32 m0, s46
	s_nop 0
	global_load_lds_dwordx4 v[12:13], off
	s_waitcnt vmcnt(8)
	s_waitcnt lgkmcnt(0)
	s_setprio 1
	v_mfma_scale_f32_16x16x128_f8f6f4 v[74:77], v[2:9], v[210:217], v[74:77], v199, v199 op_sel_hi:[0,0,0]
	v_mfma_scale_f32_16x16x128_f8f6f4 v[70:73], v[142:149], v[210:217], v[70:73], v199, v199 op_sel_hi:[0,0,0]
	v_mfma_scale_f32_16x16x128_f8f6f4 v[66:69], v[2:9], v[218:225], v[66:69], v199, v199 op_sel_hi:[0,0,0]
	v_mfma_scale_f32_16x16x128_f8f6f4 v[62:65], v[142:149], v[218:225], v[62:65], v199, v199 op_sel_hi:[0,0,0]
	v_mfma_scale_f32_16x16x128_f8f6f4 v[58:61], v[2:9], v[226:233], v[58:61], v199, v199 op_sel_hi:[0,0,0]
	v_mfma_scale_f32_16x16x128_f8f6f4 v[54:57], v[142:149], v[226:233], v[54:57], v199, v199 op_sel_hi:[0,0,0]
	v_mfma_scale_f32_16x16x128_f8f6f4 v[50:53], v[2:9], v[234:241], v[50:53], v199, v199 op_sel_hi:[0,0,0]
	v_mfma_scale_f32_16x16x128_f8f6f4 v[46:49], v[142:149], v[234:241], v[46:49], v199, v199 op_sel_hi:[0,0,0]
	s_nop 3
	s_setprio 0
	s_setprio 1
	v_mfma_scale_f32_16x16x128_f8f6f4 v[42:45], v[150:157], v[210:217], v[42:45], v199, v199 op_sel_hi:[0,0,0]
	v_mfma_scale_f32_16x16x128_f8f6f4 v[38:41], v[202:209], v[210:217], v[38:41], v199, v199 op_sel_hi:[0,0,0]
	v_mfma_scale_f32_16x16x128_f8f6f4 v[34:37], v[150:157], v[218:225], v[34:37], v199, v199 op_sel_hi:[0,0,0]
	v_mfma_scale_f32_16x16x128_f8f6f4 v[30:33], v[202:209], v[218:225], v[30:33], v199, v199 op_sel_hi:[0,0,0]
	v_mfma_scale_f32_16x16x128_f8f6f4 v[26:29], v[150:157], v[226:233], v[26:29], v199, v199 op_sel_hi:[0,0,0]
	v_mfma_scale_f32_16x16x128_f8f6f4 v[22:25], v[202:209], v[226:233], v[22:25], v199, v199 op_sel_hi:[0,0,0]
	v_mfma_scale_f32_16x16x128_f8f6f4 v[18:21], v[150:157], v[234:241], v[18:21], v199, v199 op_sel_hi:[0,0,0]
	v_mfma_scale_f32_16x16x128_f8f6f4 v[14:17], v[202:209], v[234:241], v[14:17], v199, v199 op_sel_hi:[0,0,0]
	s_setprio 0
	s_barrier
; #define PG8_STAGE(bufoff, gbase, voff) do { _Pragma("unroll") for (int _i = 0; _i < 2; ++_i) \
;         __builtin_amdgcn_global_load_lds((const unsigned*)((const char*)(gbase) + (voff)[_i]), (PG8_LAS unsigned*)(lds + (bufoff) + ldsw + _i * 8192), 16, 0, 0); } while (0)
; #define PG8_WAIT_V(n) asm volatile("s_waitcnt vmcnt(" #n ")" ::: "memory")
; #define PG8_WAIT_L(n) asm volatile("s_waitcnt lgkmcnt(" #n ")" ::: "memory")
; #define PG8_BAR __builtin_amdgcn_s_barrier()
; #define PG8_SCHED __builtin_amdgcn_sched_barrier(0)
; template <class Epi, class Sched, bool ALIGN_EPI = true, bool F8 = false>
; __device__ __forceinline__ void gemm_phase(PG8_LAS unsigned char* lds, const Sched& S, const Epi& E) {
;     ...
;             PG8_LDB(B0, 1, 0); PG8_LDB(B1, 1, 1); PG8_SCHED; PG8_LDA(At, 1, 0); PG8_STAGE(PG8_SA(0, 1), a2, vA2[1]);
;             PG8_WAIT_V(8); PG8_WAIT_L(0); PG8_BAR; PG8_MMA(0, 0, At, B0); PG8_MMA(0, 1, At, B1); PG8_BAR; PG8_SCHED;
;             PG8_LDA(At, 1, 1); PG8_STAGE(PG8_SB(1, 0), b3, voffB[0]); PG8_STAGE(PG8_SB(1, 1), b3, voffB[1]); PG8_STAGE(PG8_SA(1, 0), a3, vA2[0]);
;             PG8_WAIT_V(8); PG8_WAIT_L(0); PG8_BAR; PG8_MMA(1, 0, At, B0); PG8_MMA(1, 1, At, B1); PG8_BAR; PG8_SCHED;
	s_add_i32 s78, 0, 0x18000
	s_add_i32 s79, 0, 0x1c000
	v_add_u32_e32 v2, s78, v190
	v_add_u32_e32 v10, s79, v190
	ds_read_b128 v[142:145], v2
	ds_read_b128 v[146:149], v2 offset:1024
	ds_read_b128 v[150:153], v2 offset:2048
	ds_read_b128 v[154:157], v2 offset:3072
	ds_read_b128 v[2:5], v10
	ds_read_b128 v[6:9], v10 offset:1024
	ds_read_b128 v[202:205], v10 offset:2048
	ds_read_b128 v[206:209], v10 offset:3072
	s_mov_b32 m0, s47
	v_lshl_add_u64 v[12:13], s[30:31], 0, v[166:167]
	ds_read_b128 v[210:213], v198 offset:32768
	ds_read_b128 v[214:217], v198 offset:33792
	ds_read_b128 v[218:221], v198 offset:34816
	ds_read_b128 v[222:225], v198 offset:35840
	ds_read_b128 v[226:229], v198 offset:36864
	ds_read_b128 v[230:233], v198 offset:37888
	ds_read_b128 v[234:237], v198 offset:38912
	ds_read_b128 v[238:241], v198 offset:39936
	global_load_lds_dwordx4 v[12:13], off
	v_lshl_add_u64 v[12:13], s[30:31], 0, v[168:169]
	s_mov_b32 m0, s48
	s_nop 0
	global_load_lds_dwordx4 v[12:13], off
	s_waitcnt vmcnt(8)
	s_waitcnt lgkmcnt(0)
	s_setprio 1
	v_mfma_scale_f32_16x16x128_f8f6f4 v[138:141], v[142:149], v[210:217], v[138:141], v199, v199 op_sel_hi:[0,0,0]
	v_mfma_scale_f32_16x16x128_f8f6f4 v[134:137], v[150:157], v[210:217], v[134:137], v199, v199 op_sel_hi:[0,0,0]
	v_mfma_scale_f32_16x16x128_f8f6f4 v[130:133], v[142:149], v[218:225], v[130:133], v199, v199 op_sel_hi:[0,0,0]
	v_mfma_scale_f32_16x16x128_f8f6f4 v[126:129], v[150:157], v[218:225], v[126:129], v199, v199 op_sel_hi:[0,0,0]
	v_mfma_scale_f32_16x16x128_f8f6f4 v[122:125], v[142:149], v[226:233], v[122:125], v199, v199 op_sel_hi:[0,0,0]
	v_mfma_scale_f32_16x16x128_f8f6f4 v[118:121], v[150:157], v[226:233], v[118:121], v199, v199 op_sel_hi:[0,0,0]
	v_mfma_scale_f32_16x16x128_f8f6f4 v[114:117], v[142:149], v[234:241], v[114:117], v199, v199 op_sel_hi:[0,0,0]
	v_mfma_scale_f32_16x16x128_f8f6f4 v[110:113], v[150:157], v[234:241], v[110:113], v199, v199 op_sel_hi:[0,0,0]
	s_nop 3
	s_setprio 0
	s_setprio 1
	v_mfma_scale_f32_16x16x128_f8f6f4 v[106:109], v[2:9], v[210:217], v[106:109], v199, v199 op_sel_hi:[0,0,0]
	v_mfma_scale_f32_16x16x128_f8f6f4 v[102:105], v[202:209], v[210:217], v[102:105], v199, v199 op_sel_hi:[0,0,0]
	v_mfma_scale_f32_16x16x128_f8f6f4 v[98:101], v[2:9], v[218:225], v[98:101], v199, v199 op_sel_hi:[0,0,0]
	v_mfma_scale_f32_16x16x128_f8f6f4 v[94:97], v[202:209], v[218:225], v[94:97], v199, v199 op_sel_hi:[0,0,0]
	v_mfma_scale_f32_16x16x128_f8f6f4 v[90:93], v[2:9], v[226:233], v[90:93], v199, v199 op_sel_hi:[0,0,0]
	v_mfma_scale_f32_16x16x128_f8f6f4 v[86:89], v[202:209], v[226:233], v[86:89], v199, v199 op_sel_hi:[0,0,0]
	v_mfma_scale_f32_16x16x128_f8f6f4 v[82:85], v[2:9], v[234:241], v[82:85], v199, v199 op_sel_hi:[0,0,0]
	v_mfma_scale_f32_16x16x128_f8f6f4 v[78:81], v[202:209], v[234:241], v[78:81], v199, v199 op_sel_hi:[0,0,0]
	s_setprio 0
	s_barrier
	s_add_u32 s28, s28, 0x8000
	s_addc_u32 s29, s29, 0
	s_add_i32 s30, s78, s44
	v_lshl_add_u64 v[12:13], s[28:29], 0, v[158:159]
	s_mov_b32 m0, s30
	ds_read_b128 v[210:213], v198 offset:49152
	ds_read_b128 v[214:217], v198 offset:50176
	ds_read_b128 v[218:221], v198 offset:51200
	ds_read_b128 v[222:225], v198 offset:52224
	ds_read_b128 v[226:229], v198 offset:53248
	ds_read_b128 v[230:233], v198 offset:54272
	ds_read_b128 v[234:237], v198 offset:55296
	ds_read_b128 v[238:241], v198 offset:56320
	global_load_lds_dwordx4 v[12:13], off
	v_lshl_add_u64 v[12:13], s[28:29], 0, v[160:161]
	s_add_i32 m0, s30, 0x2000
	s_add_i32 s30, s79, s44
	global_load_lds_dwordx4 v[12:13], off
	v_lshl_add_u64 v[12:13], s[28:29], 0, v[172:173]
	s_mov_b32 m0, s30
	s_nop 0
	global_load_lds_dwordx4 v[12:13], off
	v_lshl_add_u64 v[12:13], s[28:29], 0, v[174:175]
	s_add_i32 m0, s30, 0x2000
	s_nop 0
	global_load_lds_dwordx4 v[12:13], off
	v_lshl_add_u64 v[12:13], s[26:27], 0, v[162:163]
	s_mov_b32 m0, s50
	s_nop 0
	global_load_lds_dwordx4 v[12:13], off
	v_lshl_add_u64 v[12:13], s[26:27], 0, v[164:165]
	s_mov_b32 m0, s51
	s_nop 0
	global_load_lds_dwordx4 v[12:13], off
	s_waitcnt vmcnt(8)
	s_waitcnt lgkmcnt(0)
	s_setprio 1
	v_mfma_scale_f32_16x16x128_f8f6f4 v[74:77], v[142:149], v[210:217], v[74:77], v199, v199 op_sel_hi:[0,0,0]
	v_mfma_scale_f32_16x16x128_f8f6f4 v[70:73], v[150:157], v[210:217], v[70:73], v199, v199 op_sel_hi:[0,0,0]
	v_mfma_scale_f32_16x16x128_f8f6f4 v[66:69], v[142:149], v[218:225], v[66:69], v199, v199 op_sel_hi:[0,0,0]
	v_mfma_scale_f32_16x16x128_f8f6f4 v[62:65], v[150:157], v[218:225], v[62:65], v199, v199 op_sel_hi:[0,0,0]
	v_mfma_scale_f32_16x16x128_f8f6f4 v[58:61], v[142:149], v[226:233], v[58:61], v199, v199 op_sel_hi:[0,0,0]
	v_mfma_scale_f32_16x16x128_f8f6f4 v[54:57], v[150:157], v[226:233], v[54:57], v199, v199 op_sel_hi:[0,0,0]
	v_mfma_scale_f32_16x16x128_f8f6f4 v[50:53], v[142:149], v[234:241], v[50:53], v199, v199 op_sel_hi:[0,0,0]
	v_mfma_scale_f32_16x16x128_f8f6f4 v[46:49], v[150:157], v[234:241], v[46:49], v199, v199 op_sel_hi:[0,0,0]
	s_nop 3
	s_setprio 0
	s_setprio 1
	v_mfma_scale_f32_16x16x128_f8f6f4 v[42:45], v[2:9], v[210:217], v[42:45], v199, v199 op_sel_hi:[0,0,0]
	v_mfma_scale_f32_16x16x128_f8f6f4 v[38:41], v[202:209], v[210:217], v[38:41], v199, v199 op_sel_hi:[0,0,0]
	v_mfma_scale_f32_16x16x128_f8f6f4 v[34:37], v[2:9], v[218:225], v[34:37], v199, v199 op_sel_hi:[0,0,0]
	v_mfma_scale_f32_16x16x128_f8f6f4 v[30:33], v[202:209], v[218:225], v[30:33], v199, v199 op_sel_hi:[0,0,0]
	v_mfma_scale_f32_16x16x128_f8f6f4 v[26:29], v[2:9], v[226:233], v[26:29], v199, v199 op_sel_hi:[0,0,0]
	v_mfma_scale_f32_16x16x128_f8f6f4 v[22:25], v[202:209], v[226:233], v[22:25], v199, v199 op_sel_hi:[0,0,0]
	v_mfma_scale_f32_16x16x128_f8f6f4 v[18:21], v[2:9], v[234:241], v[18:21], v199, v199 op_sel_hi:[0,0,0]
	v_mfma_scale_f32_16x16x128_f8f6f4 v[14:17], v[202:209], v[234:241], v[14:17], v199, v199 op_sel_hi:[0,0,0]
	s_setprio 0
	s_barrier
	s_add_u32 s75, s75, 0x10000
	s_addc_u32 s76, s76, 0
	s_add_u32 s24, s24, 0x10000
	s_addc_u32 s25, s25, 0
	s_cmp_ge_i32 s77, s72
	s_mov_b32 s26, s77
	s_cbranch_scc0 .LBB0_834
	s_branch .Lfx_23459
	.p2align	6

; #define PG8_STAGE(bufoff, gbase, voff) do { _Pragma("unroll") for (int _i = 0; _i < 2; ++_i) \
;         __builtin_amdgcn_global_load_lds((const unsigned*)((const char*)(gbase) + (voff)[_i]), (PG8_LAS unsigned*)(lds + (bufoff) + ldsw + _i * 8192), 16, 0, 0); } while (0)
; #define PG8_WAIT_V(n) asm volatile("s_waitcnt vmcnt(" #n ")" ::: "memory")
; #define PG8_WAIT_L(n) asm volatile("s_waitcnt lgkmcnt(" #n ")" ::: "memory")
; #define PG8_BAR __builtin_amdgcn_s_barrier()
; #define PG8_SCHED __builtin_amdgcn_sched_barrier(0)
; template <class Epi, class Sched, bool ALIGN_EPI = true, bool F8 = false>
; __device__ __forceinline__ void gemm_phase(PG8_LAS unsigned char* lds, const Sched& S, const Epi& E) {
;     ...
;             PG8_LDB(B0, 0, 0); PG8_LDB(B1, 0, 1); PG8_SCHED; PG8_LDA(At, 0, 0); PG8_STAGE(PG8_SA(1, 1), a1, voffA[1]);
;             PG8_WAIT_V(8); PG8_WAIT_L(0); PG8_BAR; PG8_MMA(0, 0, At, B0); PG8_MMA(0, 1, At, B1); PG8_BAR; PG8_SCHED;
;             PG8_LDA(At, 0, 1); PG8_STAGE(PG8_SB(0, 0), b2, voffB[0]); PG8_STAGE(PG8_SB(0, 1), b2, voffB[1]); PG8_STAGE(PG8_SA(0, 0), a2, vA2[0]);
;             PG8_WAIT_V(8); PG8_WAIT_L(0); PG8_BAR; PG8_MMA(1, 0, At, B0); PG8_MMA(1, 1, At, B1); PG8_BAR; PG8_SCHED;
;     ...
; #pragma unroll
;         for (int a = 0; a < 2; ++a)
; #pragma unroll
;             for (int b = 0; b < 2; ++b)
; #pragma unroll
;                 for (int m = 0; m < 4; ++m)
; #pragma unroll
;                     for (int n = 0; n < 2; ++n) acc[a][b][m][n] = (f32x4){0.f, 0.f, 0.f, 0.f};
;         }
;         cur = nxt; cA = nA; cB = nB; ++ui;
; #pragma unroll
;         for (int h = 0; h < 2; ++h)
; #pragma unroll
;             for (int i = 0; i < 2; ++i) voffA[h][i] = voffAn[h][i];
.LBB0_910:
	s_add_u32 s19, s30, 0x10000
	s_addc_u32 s21, s31, 0
	s_add_u32 s28, s28, 0x8000
	v_mov_b64_e32 v[34:35], 0
	s_addc_u32 s29, s29, 0
	s_mov_b32 s65, -2
	v_mov_b64_e32 v[36:37], 0
	v_mov_b64_e32 v[38:39], 0
	v_mov_b64_e32 v[40:41], 0
	v_mov_b64_e32 v[46:47], 0
	v_mov_b64_e32 v[48:49], 0
	v_mov_b64_e32 v[54:55], 0
	v_mov_b64_e32 v[56:57], 0
	v_mov_b64_e32 v[62:63], 0
	v_mov_b64_e32 v[64:65], 0
	v_mov_b64_e32 v[70:71], 0
	v_mov_b64_e32 v[72:73], 0
	v_mov_b64_e32 v[78:79], 0
	v_mov_b64_e32 v[80:81], 0
	v_mov_b64_e32 v[86:87], 0
	v_mov_b64_e32 v[88:89], 0
	v_mov_b64_e32 v[42:43], 0
	v_mov_b64_e32 v[44:45], 0
	v_mov_b64_e32 v[50:51], 0
	v_mov_b64_e32 v[52:53], 0
	v_mov_b64_e32 v[58:59], 0
	v_mov_b64_e32 v[60:61], 0
	v_mov_b64_e32 v[66:67], 0
	v_mov_b64_e32 v[68:69], 0
	v_mov_b64_e32 v[74:75], 0
	v_mov_b64_e32 v[76:77], 0
	v_mov_b64_e32 v[82:83], 0
	v_mov_b64_e32 v[84:85], 0
	v_mov_b64_e32 v[90:91], 0
	v_mov_b64_e32 v[92:93], 0
	v_mov_b64_e32 v[94:95], 0
	v_mov_b64_e32 v[96:97], 0
	v_mov_b64_e32 v[98:99], 0
	v_mov_b64_e32 v[100:101], 0
	v_mov_b64_e32 v[102:103], 0
	v_mov_b64_e32 v[104:105], 0
	v_mov_b64_e32 v[110:111], 0
	v_mov_b64_e32 v[112:113], 0
	v_mov_b64_e32 v[118:119], 0
	v_mov_b64_e32 v[120:121], 0
	v_mov_b64_e32 v[126:127], 0
	v_mov_b64_e32 v[128:129], 0
	v_mov_b64_e32 v[134:135], 0
	v_mov_b64_e32 v[136:137], 0
	v_mov_b64_e32 v[138:139], 0
	v_mov_b64_e32 v[140:141], 0
	v_mov_b64_e32 v[142:143], 0
	v_mov_b64_e32 v[144:145], 0
	v_mov_b64_e32 v[106:107], 0
	v_mov_b64_e32 v[108:109], 0
	v_mov_b64_e32 v[114:115], 0
	v_mov_b64_e32 v[116:117], 0
	v_mov_b64_e32 v[122:123], 0
	v_mov_b64_e32 v[124:125], 0
	v_mov_b64_e32 v[130:131], 0
	v_mov_b64_e32 v[132:133], 0
	v_mov_b64_e32 v[146:147], 0
	v_mov_b64_e32 v[148:149], 0
	v_mov_b64_e32 v[150:151], 0
	v_mov_b64_e32 v[152:153], 0
	v_mov_b64_e32 v[154:155], 0
	v_mov_b64_e32 v[156:157], 0
	v_mov_b64_e32 v[158:159], 0
	v_mov_b64_e32 v[160:161], 0
	s_bitcmp1_b32 s3, 2
	s_cbranch_scc1 .Lh1e_26630
	.p2align	6
.LBB0_911:
	ds_read_b128 v[18:21], v191
	ds_read_b128 v[22:25], v191 offset:1024
	ds_read_b128 v[26:29], v191 offset:2048
	ds_read_b128 v[30:33], v191 offset:3072
	ds_read_b128 v[2:5], v192
	ds_read_b128 v[6:9], v192 offset:1024
	ds_read_b128 v[10:13], v192 offset:2048
	ds_read_b128 v[14:17], v192 offset:3072
	s_add_u32 s30, s28, 0x8000
	s_addc_u32 s31, s29, 0
	s_cmp_eq_u32 s65, 12
	s_cselect_b32 s42, s22, s30
	s_cselect_b32 s43, s23, s31
	s_cselect_b32 s40, s24, s19
	s_cselect_b32 s41, s25, s21
	s_add_u32 s30, s42, 0x8000
	s_addc_u32 s31, s43, 0
	v_lshl_add_u64 v[228:229], s[28:29], 0, v[182:183]
	s_add_i32 m0, s27, 0xc000
	ds_read_b128 v[196:199], v193
	ds_read_b128 v[200:203], v193 offset:1024
	ds_read_b128 v[204:207], v193 offset:2048
	ds_read_b128 v[208:211], v193 offset:3072
	ds_read_b128 v[212:215], v193 offset:4096
	ds_read_b128 v[216:219], v193 offset:5120
	ds_read_b128 v[220:223], v193 offset:6144
	ds_read_b128 v[224:227], v193 offset:7168
	global_load_lds_dwordx4 v[228:229], off
	v_lshl_add_u64 v[228:229], s[28:29], 0, v[180:181]
	s_add_i32 m0, s27, 0xe000
	s_nop 0
	global_load_lds_dwordx4 v[228:229], off
	s_waitcnt vmcnt(8)
	s_waitcnt lgkmcnt(0)
	s_setprio 1
	v_mfma_scale_f32_16x16x128_f8f6f4 v[158:161], v[18:25], v[196:203], v[158:161], v194, v194 op_sel_hi:[0,0,0]
	v_mfma_scale_f32_16x16x128_f8f6f4 v[154:157], v[26:33], v[196:203], v[154:157], v194, v194 op_sel_hi:[0,0,0]
	v_mfma_scale_f32_16x16x128_f8f6f4 v[150:153], v[18:25], v[204:211], v[150:153], v194, v194 op_sel_hi:[0,0,0]
	v_mfma_scale_f32_16x16x128_f8f6f4 v[146:149], v[26:33], v[204:211], v[146:149], v194, v194 op_sel_hi:[0,0,0]
	v_mfma_scale_f32_16x16x128_f8f6f4 v[130:133], v[18:25], v[212:219], v[130:133], v194, v194 op_sel_hi:[0,0,0]
	v_mfma_scale_f32_16x16x128_f8f6f4 v[122:125], v[26:33], v[212:219], v[122:125], v194, v194 op_sel_hi:[0,0,0]
	v_mfma_scale_f32_16x16x128_f8f6f4 v[114:117], v[18:25], v[220:227], v[114:117], v194, v194 op_sel_hi:[0,0,0]
	v_mfma_scale_f32_16x16x128_f8f6f4 v[106:109], v[26:33], v[220:227], v[106:109], v194, v194 op_sel_hi:[0,0,0]
	s_nop 3
	s_setprio 0
	s_setprio 1
	v_mfma_scale_f32_16x16x128_f8f6f4 v[142:145], v[2:9], v[196:203], v[142:145], v194, v194 op_sel_hi:[0,0,0]
	v_mfma_scale_f32_16x16x128_f8f6f4 v[138:141], v[10:17], v[196:203], v[138:141], v194, v194 op_sel_hi:[0,0,0]
	v_mfma_scale_f32_16x16x128_f8f6f4 v[134:137], v[2:9], v[204:211], v[134:137], v194, v194 op_sel_hi:[0,0,0]
	v_mfma_scale_f32_16x16x128_f8f6f4 v[126:129], v[10:17], v[204:211], v[126:129], v194, v194 op_sel_hi:[0,0,0]
	v_mfma_scale_f32_16x16x128_f8f6f4 v[118:121], v[2:9], v[212:219], v[118:121], v194, v194 op_sel_hi:[0,0,0]
	v_mfma_scale_f32_16x16x128_f8f6f4 v[110:113], v[10:17], v[212:219], v[110:113], v194, v194 op_sel_hi:[0,0,0]
	v_mfma_scale_f32_16x16x128_f8f6f4 v[102:105], v[2:9], v[220:227], v[102:105], v194, v194 op_sel_hi:[0,0,0]
	v_mfma_scale_f32_16x16x128_f8f6f4 v[98:101], v[10:17], v[220:227], v[98:101], v194, v194 op_sel_hi:[0,0,0]
	s_setprio 0
	s_barrier
; #define PG8_STAGE(bufoff, gbase, voff) do { _Pragma("unroll") for (int _i = 0; _i < 2; ++_i) \
;         __builtin_amdgcn_global_load_lds((const unsigned*)((const char*)(gbase) + (voff)[_i]), (PG8_LAS unsigned*)(lds + (bufoff) + ldsw + _i * 8192), 16, 0, 0); } while (0)
; #define PG8_WAIT_V(n) asm volatile("s_waitcnt vmcnt(" #n ")" ::: "memory")
; #define PG8_WAIT_L(n) asm volatile("s_waitcnt lgkmcnt(" #n ")" ::: "memory")
; #define PG8_BAR __builtin_amdgcn_s_barrier()
; #define PG8_SCHED __builtin_amdgcn_sched_barrier(0)
; template <class Epi, class Sched, bool ALIGN_EPI = true, bool F8 = false>
; __device__ __forceinline__ void gemm_phase(PG8_LAS unsigned char* lds, const Sched& S, const Epi& E) {
;     ...
;             PG8_LDA(At, 0, 1); PG8_STAGE(PG8_SB(0, 0), b2, voffB[0]); PG8_STAGE(PG8_SB(0, 1), b2, voffB[1]); PG8_STAGE(PG8_SA(0, 0), a2, vA2[0]);
;             PG8_WAIT_V(8); PG8_WAIT_L(0); PG8_BAR; PG8_MMA(1, 0, At, B0); PG8_MMA(1, 1, At, B1); PG8_BAR; PG8_SCHED;
;             PG8_LDB(B0, 1, 0); PG8_LDB(B1, 1, 1); PG8_SCHED; PG8_LDA(At, 1, 0); PG8_STAGE(PG8_SA(0, 1), a2, vA2[1]);
;             PG8_WAIT_V(8); PG8_WAIT_L(0); PG8_BAR; PG8_MMA(0, 0, At, B0); PG8_MMA(0, 1, At, B1); PG8_BAR; PG8_SCHED;
	s_add_i32 s66, s60, s48
	v_lshl_add_u64 v[228:229], s[40:41], 0, v[162:163]
	s_mov_b32 m0, s66
	ds_read_b128 v[196:199], v193 offset:16384
	ds_read_b128 v[200:203], v193 offset:17408
	ds_read_b128 v[204:207], v193 offset:18432
	ds_read_b128 v[208:211], v193 offset:19456
	ds_read_b128 v[212:215], v193 offset:20480
	ds_read_b128 v[216:219], v193 offset:21504
	ds_read_b128 v[220:223], v193 offset:22528
	ds_read_b128 v[224:227], v193 offset:23552
	global_load_lds_dwordx4 v[228:229], off
	v_lshl_add_u64 v[230:231], s[40:41], 0, v[164:165]
	s_add_i32 m0, s66, 0x2000
	s_add_i32 s66, s61, s48
	global_load_lds_dwordx4 v[230:231], off
	v_lshl_add_u64 v[228:229], v[228:229], 0, s[6:7]
	s_mov_b32 m0, s66
	s_nop 0
	global_load_lds_dwordx4 v[228:229], off
	v_lshl_add_u64 v[228:229], v[230:231], 0, s[6:7]
	s_add_i32 m0, s66, 0x2000
	s_nop 0
	global_load_lds_dwordx4 v[228:229], off
	v_lshl_add_u64 v[228:229], s[42:43], 0, v[166:167]
	s_mov_b32 m0, s27
	s_nop 0
	global_load_lds_dwordx4 v[228:229], off
	v_lshl_add_u64 v[228:229], s[42:43], 0, v[168:169]
	s_mov_b32 m0, s49
	s_nop 0
	global_load_lds_dwordx4 v[228:229], off
	s_waitcnt vmcnt(8)
	s_waitcnt lgkmcnt(0)
	s_setprio 1
	v_mfma_scale_f32_16x16x128_f8f6f4 v[94:97], v[18:25], v[196:203], v[94:97], v194, v194 op_sel_hi:[0,0,0]
	v_mfma_scale_f32_16x16x128_f8f6f4 v[90:93], v[26:33], v[196:203], v[90:93], v194, v194 op_sel_hi:[0,0,0]
	v_mfma_scale_f32_16x16x128_f8f6f4 v[82:85], v[18:25], v[204:211], v[82:85], v194, v194 op_sel_hi:[0,0,0]
	v_mfma_scale_f32_16x16x128_f8f6f4 v[74:77], v[26:33], v[204:211], v[74:77], v194, v194 op_sel_hi:[0,0,0]
	v_mfma_scale_f32_16x16x128_f8f6f4 v[66:69], v[18:25], v[212:219], v[66:69], v194, v194 op_sel_hi:[0,0,0]
	v_mfma_scale_f32_16x16x128_f8f6f4 v[58:61], v[26:33], v[212:219], v[58:61], v194, v194 op_sel_hi:[0,0,0]
	v_mfma_scale_f32_16x16x128_f8f6f4 v[50:53], v[18:25], v[220:227], v[50:53], v194, v194 op_sel_hi:[0,0,0]
	v_mfma_scale_f32_16x16x128_f8f6f4 v[42:45], v[26:33], v[220:227], v[42:45], v194, v194 op_sel_hi:[0,0,0]
	s_nop 3
	s_setprio 0
	s_setprio 1
	v_mfma_scale_f32_16x16x128_f8f6f4 v[86:89], v[2:9], v[196:203], v[86:89], v194, v194 op_sel_hi:[0,0,0]
	v_mfma_scale_f32_16x16x128_f8f6f4 v[78:81], v[10:17], v[196:203], v[78:81], v194, v194 op_sel_hi:[0,0,0]
	v_mfma_scale_f32_16x16x128_f8f6f4 v[70:73], v[2:9], v[204:211], v[70:73], v194, v194 op_sel_hi:[0,0,0]
	v_mfma_scale_f32_16x16x128_f8f6f4 v[62:65], v[10:17], v[204:211], v[62:65], v194, v194 op_sel_hi:[0,0,0]
	v_mfma_scale_f32_16x16x128_f8f6f4 v[54:57], v[2:9], v[212:219], v[54:57], v194, v194 op_sel_hi:[0,0,0]
	v_mfma_scale_f32_16x16x128_f8f6f4 v[46:49], v[10:17], v[212:219], v[46:49], v194, v194 op_sel_hi:[0,0,0]
	v_mfma_scale_f32_16x16x128_f8f6f4 v[38:41], v[2:9], v[220:227], v[38:41], v194, v194 op_sel_hi:[0,0,0]
	v_mfma_scale_f32_16x16x128_f8f6f4 v[34:37], v[10:17], v[220:227], v[34:37], v194, v194 op_sel_hi:[0,0,0]
	s_setprio 0
	s_barrier
	s_add_i32 s66, 0, 0x18000
	s_add_i32 s67, 0, 0x1c000
	v_add_u32_e32 v14, s66, v189
	v_add_u32_e32 v30, s67, v189
	ds_read_b128 v[2:5], v14
	ds_read_b128 v[6:9], v14 offset:1024
	ds_read_b128 v[10:13], v14 offset:2048
	ds_read_b128 v[14:17], v14 offset:3072
	ds_read_b128 v[18:21], v30
	ds_read_b128 v[22:25], v30 offset:1024
	ds_read_b128 v[26:29], v30 offset:2048
	ds_read_b128 v[30:33], v30 offset:3072
	s_mov_b32 m0, s50
	v_lshl_add_u64 v[228:229], s[42:43], 0, v[172:173]
	ds_read_b128 v[196:199], v193 offset:32768
	ds_read_b128 v[200:203], v193 offset:33792
	ds_read_b128 v[204:207], v193 offset:34816
	ds_read_b128 v[208:211], v193 offset:35840
	ds_read_b128 v[212:215], v193 offset:36864
	ds_read_b128 v[216:219], v193 offset:37888
	ds_read_b128 v[220:223], v193 offset:38912
	ds_read_b128 v[224:227], v193 offset:39936
	global_load_lds_dwordx4 v[228:229], off
	v_lshl_add_u64 v[228:229], s[42:43], 0, v[174:175]
	s_mov_b32 m0, s51
	s_nop 0
	global_load_lds_dwordx4 v[228:229], off
	s_waitcnt vmcnt(8)
	s_waitcnt lgkmcnt(0)
	s_setprio 1
	v_mfma_scale_f32_16x16x128_f8f6f4 v[158:161], v[2:9], v[196:203], v[158:161], v194, v194 op_sel_hi:[0,0,0]
	v_mfma_scale_f32_16x16x128_f8f6f4 v[154:157], v[10:17], v[196:203], v[154:157], v194, v194 op_sel_hi:[0,0,0]
	v_mfma_scale_f32_16x16x128_f8f6f4 v[150:153], v[2:9], v[204:211], v[150:153], v194, v194 op_sel_hi:[0,0,0]
	v_mfma_scale_f32_16x16x128_f8f6f4 v[146:149], v[10:17], v[204:211], v[146:149], v194, v194 op_sel_hi:[0,0,0]
	v_mfma_scale_f32_16x16x128_f8f6f4 v[130:133], v[2:9], v[212:219], v[130:133], v194, v194 op_sel_hi:[0,0,0]
	v_mfma_scale_f32_16x16x128_f8f6f4 v[122:125], v[10:17], v[212:219], v[122:125], v194, v194 op_sel_hi:[0,0,0]
	v_mfma_scale_f32_16x16x128_f8f6f4 v[114:117], v[2:9], v[220:227], v[114:117], v194, v194 op_sel_hi:[0,0,0]
	v_mfma_scale_f32_16x16x128_f8f6f4 v[106:109], v[10:17], v[220:227], v[106:109], v194, v194 op_sel_hi:[0,0,0]
	s_nop 3
	s_setprio 0
	s_setprio 1
	v_mfma_scale_f32_16x16x128_f8f6f4 v[142:145], v[18:25], v[196:203], v[142:145], v194, v194 op_sel_hi:[0,0,0]
	v_mfma_scale_f32_16x16x128_f8f6f4 v[138:141], v[26:33], v[196:203], v[138:141], v194, v194 op_sel_hi:[0,0,0]
	v_mfma_scale_f32_16x16x128_f8f6f4 v[134:137], v[18:25], v[204:211], v[134:137], v194, v194 op_sel_hi:[0,0,0]
	v_mfma_scale_f32_16x16x128_f8f6f4 v[126:129], v[26:33], v[204:211], v[126:129], v194, v194 op_sel_hi:[0,0,0]
	v_mfma_scale_f32_16x16x128_f8f6f4 v[118:121], v[18:25], v[212:219], v[118:121], v194, v194 op_sel_hi:[0,0,0]
	v_mfma_scale_f32_16x16x128_f8f6f4 v[110:113], v[26:33], v[212:219], v[110:113], v194, v194 op_sel_hi:[0,0,0]
	v_mfma_scale_f32_16x16x128_f8f6f4 v[102:105], v[18:25], v[220:227], v[102:105], v194, v194 op_sel_hi:[0,0,0]
	v_mfma_scale_f32_16x16x128_f8f6f4 v[98:101], v[26:33], v[220:227], v[98:101], v194, v194 op_sel_hi:[0,0,0]
	s_setprio 0
	s_barrier
; #define PG8_STAGE(bufoff, gbase, voff) do { _Pragma("unroll") for (int _i = 0; _i < 2; ++_i) \
;         __builtin_amdgcn_global_load_lds((const unsigned*)((const char*)(gbase) + (voff)[_i]), (PG8_LAS unsigned*)(lds + (bufoff) + ldsw + _i * 8192), 16, 0, 0); } while (0)
; #define PG8_WAIT_V(n) asm volatile("s_waitcnt vmcnt(" #n ")" ::: "memory")
; #define PG8_WAIT_L(n) asm volatile("s_waitcnt lgkmcnt(" #n ")" ::: "memory")
; #define PG8_BAR __builtin_amdgcn_s_barrier()
; #define PG8_SCHED __builtin_amdgcn_sched_barrier(0)
; template <class Epi, class Sched, bool ALIGN_EPI = true, bool F8 = false>
; __device__ __forceinline__ void gemm_phase(PG8_LAS unsigned char* lds, const Sched& S, const Epi& E) {
;     ...
;             PG8_LDA(At, 1, 1); PG8_STAGE(PG8_SB(1, 0), b3, voffB[0]); PG8_STAGE(PG8_SB(1, 1), b3, voffB[1]); PG8_STAGE(PG8_SA(1, 0), a3, vA2[0]);
;             PG8_WAIT_V(8); PG8_WAIT_L(0); PG8_BAR; PG8_MMA(1, 0, At, B0); PG8_MMA(1, 1, At, B1); PG8_BAR; PG8_SCHED;
	s_add_u32 s40, s40, 0x8000
	s_addc_u32 s41, s41, 0
	s_add_i32 s42, s66, s48
	v_lshl_add_u64 v[228:229], s[40:41], 0, v[162:163]
	s_mov_b32 m0, s42
	ds_read_b128 v[196:199], v193 offset:49152
	ds_read_b128 v[200:203], v193 offset:50176
	ds_read_b128 v[204:207], v193 offset:51200
	ds_read_b128 v[208:211], v193 offset:52224
	ds_read_b128 v[212:215], v193 offset:53248
	ds_read_b128 v[216:219], v193 offset:54272
	ds_read_b128 v[220:223], v193 offset:55296
	ds_read_b128 v[224:227], v193 offset:56320
	global_load_lds_dwordx4 v[228:229], off
	v_lshl_add_u64 v[228:229], s[40:41], 0, v[164:165]
	s_add_i32 m0, s42, 0x2000
	s_add_i32 s42, s67, s48
	global_load_lds_dwordx4 v[228:229], off
	v_lshl_add_u64 v[228:229], s[40:41], 0, v[176:177]
	s_mov_b32 m0, s42
	s_nop 0
	global_load_lds_dwordx4 v[228:229], off
	v_lshl_add_u64 v[228:229], s[40:41], 0, v[178:179]
	s_add_i32 m0, s42, 0x2000
	s_nop 0
	global_load_lds_dwordx4 v[228:229], off
	v_lshl_add_u64 v[228:229], s[30:31], 0, v[166:167]
	s_mov_b32 m0, s53
	s_nop 0
	global_load_lds_dwordx4 v[228:229], off
	v_lshl_add_u64 v[228:229], s[30:31], 0, v[168:169]
	s_mov_b32 m0, s58
	s_nop 0
	global_load_lds_dwordx4 v[228:229], off
	s_waitcnt vmcnt(8)
	s_waitcnt lgkmcnt(0)
	s_setprio 1
	v_mfma_scale_f32_16x16x128_f8f6f4 v[94:97], v[2:9], v[196:203], v[94:97], v194, v194 op_sel_hi:[0,0,0]
	v_mfma_scale_f32_16x16x128_f8f6f4 v[90:93], v[10:17], v[196:203], v[90:93], v194, v194 op_sel_hi:[0,0,0]
	v_mfma_scale_f32_16x16x128_f8f6f4 v[82:85], v[2:9], v[204:211], v[82:85], v194, v194 op_sel_hi:[0,0,0]
	v_mfma_scale_f32_16x16x128_f8f6f4 v[74:77], v[10:17], v[204:211], v[74:77], v194, v194 op_sel_hi:[0,0,0]
	v_mfma_scale_f32_16x16x128_f8f6f4 v[66:69], v[2:9], v[212:219], v[66:69], v194, v194 op_sel_hi:[0,0,0]
	v_mfma_scale_f32_16x16x128_f8f6f4 v[58:61], v[10:17], v[212:219], v[58:61], v194, v194 op_sel_hi:[0,0,0]
	v_mfma_scale_f32_16x16x128_f8f6f4 v[50:53], v[2:9], v[220:227], v[50:53], v194, v194 op_sel_hi:[0,0,0]
	v_mfma_scale_f32_16x16x128_f8f6f4 v[42:45], v[10:17], v[220:227], v[42:45], v194, v194 op_sel_hi:[0,0,0]
	s_nop 3
	s_setprio 0
	s_setprio 1
	v_mfma_scale_f32_16x16x128_f8f6f4 v[86:89], v[18:25], v[196:203], v[86:89], v194, v194 op_sel_hi:[0,0,0]
	v_mfma_scale_f32_16x16x128_f8f6f4 v[78:81], v[26:33], v[196:203], v[78:81], v194, v194 op_sel_hi:[0,0,0]
	v_mfma_scale_f32_16x16x128_f8f6f4 v[70:73], v[18:25], v[204:211], v[70:73], v194, v194 op_sel_hi:[0,0,0]
	v_mfma_scale_f32_16x16x128_f8f6f4 v[62:65], v[26:33], v[204:211], v[62:65], v194, v194 op_sel_hi:[0,0,0]
	v_mfma_scale_f32_16x16x128_f8f6f4 v[54:57], v[18:25], v[212:219], v[54:57], v194, v194 op_sel_hi:[0,0,0]
	v_mfma_scale_f32_16x16x128_f8f6f4 v[46:49], v[26:33], v[212:219], v[46:49], v194, v194 op_sel_hi:[0,0,0]
	v_mfma_scale_f32_16x16x128_f8f6f4 v[38:41], v[18:25], v[220:227], v[38:41], v194, v194 op_sel_hi:[0,0,0]
	v_mfma_scale_f32_16x16x128_f8f6f4 v[34:37], v[26:33], v[220:227], v[34:37], v194, v194 op_sel_hi:[0,0,0]
	s_setprio 0
	s_barrier
	s_add_i32 s65, s65, 2
	s_add_u32 s19, s19, 0x10000
	s_addc_u32 s21, s21, 0
	s_add_u32 s28, s28, 0x10000
	s_addc_u32 s29, s29, 0
	s_cmp_gt_u32 s65, 13
	s_cbranch_scc0 .LBB0_911
	s_branch .Lfx_26630
	.p2align	6

;     __device__ __forceinline__ bool next(int i, GUnit& u) const { const int L = i * G + c; const int ti = L >> 3, ct = L & 7; if (ti >= __builtin_amdgcn_readfirstlane(pre[NE])) return false;
;         int e = 0;
; #pragma unroll 1
;         for (int s = 16; s >= 1; s >>= 1) if (pre[e + s] <= ti) e += s;
;         e = __builtin_amdgcn_readfirstlane(e);
;         u.A = Abase; u.B = Bbase + ((size_t)((e * 8 + ct) * NT) << 15); u.nt = NT; u.x0 = e; u.x1 = ti - __builtin_amdgcn_readfirstlane(pre[e]); u.x2 = ct; u.x3 = __builtin_amdgcn_readfirstlane(cnt[e]); return true; }
;     __device__ __forceinline__ void a_off(const GUnit& u, const int (&R)[2], const int (&C)[2], unsigned (&v)[2][2]) const {
;         const int* rl = rowlist + (size_t)u.x0 * ECAP; const int base = u.x1 * 256, cm = u.x3 - 1;
; #pragma unroll
;         for (int h = 0; h < 2; ++h)
; #pragma unroll
;             for (int i = 0; i < 2; ++i) { int p = base + h * 128 + R[i]; p = p < cm ? p : cm; const unsigned ent = (unsigned)rl[p]; v[h][i] = (ent >> SHIFT) * (unsigned)PA + (unsigned)C[i] * 2u; } }
.LBB0_1057:
	s_ashr_i32 s21, s20, 31
	s_lshl_b64 s[28:29], s[20:21], 17
	s_lshl_b32 s21, s66, 8
	s_add_i32 s30, s65, -1
	s_or_b32 s31, s21, 0x80
	v_or_b32_e32 v2, s21, v206
	v_or_b32_e32 v4, s21, v207
	v_or_b32_e32 v6, s31, v206
	v_or_b32_e32 v8, s31, v207
	s_add_u32 s28, s46, s28
	v_min_i32_e32 v2, s30, v2
	v_min_i32_e32 v4, s30, v4
	v_min_i32_e32 v6, s30, v6
	v_min_i32_e32 v8, s30, v8
	s_addc_u32 s29, s47, s29
	v_ashrrev_i32_e32 v3, 31, v2
	v_ashrrev_i32_e32 v5, 31, v4
	v_ashrrev_i32_e32 v7, 31, v6
	v_ashrrev_i32_e32 v9, 31, v8
	v_mov_b32_e32 v177, v171
	v_mov_b32_e32 v175, v171
	s_add_u32 s21, s8, 0x10000
	v_lshl_add_u64 v[186:187], v[2:3], 2, s[28:29]
	v_lshl_add_u64 v[188:189], v[4:5], 2, s[28:29]
	v_lshl_add_u64 v[190:191], v[6:7], 2, s[28:29]
	v_lshl_add_u64 v[192:193], v[8:9], 2, s[28:29]
	s_addc_u32 s68, s9, 0
	v_lshl_add_u64 v[194:195], s[14:15], 0, v[174:175]
	v_lshl_add_u64 v[196:197], s[14:15], 0, v[176:177]
	s_mov_b32 s69, -2
	s_mov_b64 s[30:31], 0
	s_bitcmp1_b32 s3, 2
	s_cbranch_scc1 .Lh1e_31412
	.p2align	6

; #define PG8_STAGE(bufoff, gbase, voff) do { _Pragma("unroll") for (int _i = 0; _i < 2; ++_i) \
;         __builtin_amdgcn_global_load_lds((const unsigned*)((const char*)(gbase) + (voff)[_i]), (PG8_LAS unsigned*)(lds + (bufoff) + ldsw + _i * 8192), 16, 0, 0); } while (0)
; #define PG8_WAIT_V(n) asm volatile("s_waitcnt vmcnt(" #n ")" ::: "memory")
; #define PG8_WAIT_L(n) asm volatile("s_waitcnt lgkmcnt(" #n ")" ::: "memory")
; #define PG8_BAR __builtin_amdgcn_s_barrier()
; #define PG8_SCHED __builtin_amdgcn_sched_barrier(0)
; template <class Epi, class Sched, bool ALIGN_EPI = true, bool F8 = false>
; __device__ __forceinline__ void gemm_phase(PG8_LAS unsigned char* lds, const Sched& S, const Epi& E) {
;     ...
;             if constexpr (Sched::GATHER) { if (last && has_next) S.a_off(nxt, Rs, Cs, voffAn); }
;             const char* a1 = cA + (size_t)(t + 1) * kstep;
;             const char* a2 = last ? nA : cA + (size_t)(t + 2) * kstep; const char* b2 = last ? nB : cB + (size_t)(t + 2) * kstepB;
;             const char* a3 = a2 + kstep; const char* b3 = b2 + kstepB;
;             unsigned vA2[2][2];
; #pragma unroll
;             for (int h = 0; h < 2; ++h)
; #pragma unroll
;                 for (int i = 0; i < 2; ++i) { if constexpr (Sched::GATHER) vA2[h][i] = (last && has_next) ? voffAn[h][i] : voffA[h][i]; else vA2[h][i] = voffA[h][i]; }
;             PG8_LDB(B0, 0, 0); PG8_LDB(B1, 0, 1); PG8_SCHED; PG8_LDA(At, 0, 0); PG8_STAGE(PG8_SA(1, 1), a1, voffA[1]);
;             PG8_WAIT_V(8); PG8_WAIT_L(0); PG8_BAR; PG8_MMA(0, 0, At, B0); PG8_MMA(0, 1, At, B1); PG8_BAR; PG8_SCHED;
;             PG8_LDA(At, 0, 1); PG8_STAGE(PG8_SB(0, 0), b2, voffB[0]); PG8_STAGE(PG8_SB(0, 1), b2, voffB[1]); PG8_STAGE(PG8_SA(0, 0), a2, vA2[0]);
;             PG8_WAIT_V(8); PG8_WAIT_L(0); PG8_BAR; PG8_MMA(1, 0, At, B0); PG8_MMA(1, 1, At, B1); PG8_BAR; PG8_SCHED;
.LBB0_1060:
	v_add_u32_e32 v2, s12, v210
	v_add_u32_e32 v14, s62, v210
	s_add_u32 s28, s30, 0x100
	ds_read_b128 v[18:21], v2
	ds_read_b128 v[22:25], v2 offset:1024
	ds_read_b128 v[26:29], v2 offset:2048
	ds_read_b128 v[30:33], v2 offset:3072
	ds_read_b128 v[2:5], v14
	ds_read_b128 v[6:9], v14 offset:1024
	ds_read_b128 v[10:13], v14 offset:2048
	ds_read_b128 v[14:17], v14 offset:3072
	s_addc_u32 s29, s31, 0
	s_and_b64 s[42:43], s[40:41], exec
	s_cselect_b32 s42, 0, s28
	s_cselect_b32 s43, 0, s29
	s_add_u32 s42, s6, s42
	s_addc_u32 s43, s7, s43
	s_and_b64 s[40:41], s[40:41], exec
	s_cselect_b32 s41, s25, s68
	s_cselect_b32 s40, s24, s21
	v_lshl_add_u64 v[204:205], v[196:197], 0, s[30:31]
	s_add_i32 m0, s52, 0xc000
	ds_read_b128 v[222:225], v213
	ds_read_b128 v[226:229], v213 offset:1024
	ds_read_b128 v[230:233], v213 offset:2048
	ds_read_b128 v[234:237], v213 offset:3072
	ds_read_b128 v[238:241], v213 offset:4096
	ds_read_b128 v[242:245], v213 offset:5120
	ds_read_b128 v[246:249], v213 offset:6144
	ds_read_b128 v[250:253], v213 offset:7168
	global_load_lds_dwordx4 v[204:205], off
	v_lshl_add_u64 v[204:205], v[194:195], 0, s[30:31]
	s_add_i32 m0, s52, 0xe000
	s_nop 0
	global_load_lds_dwordx4 v[204:205], off
	s_waitcnt vmcnt(8)
	s_waitcnt lgkmcnt(0)
	s_setprio 1
	v_mfma_scale_f32_16x16x128_f8f6f4 v[142:145], v[18:25], v[222:229], v[142:145], v214, v214 op_sel_hi:[0,0,0]
	v_mfma_scale_f32_16x16x128_f8f6f4 v[138:141], v[26:33], v[222:229], v[138:141], v214, v214 op_sel_hi:[0,0,0]
	v_mfma_scale_f32_16x16x128_f8f6f4 v[134:137], v[18:25], v[230:237], v[134:137], v214, v214 op_sel_hi:[0,0,0]
	v_mfma_scale_f32_16x16x128_f8f6f4 v[130:133], v[26:33], v[230:237], v[130:133], v214, v214 op_sel_hi:[0,0,0]
	v_mfma_scale_f32_16x16x128_f8f6f4 v[126:129], v[18:25], v[238:245], v[126:129], v214, v214 op_sel_hi:[0,0,0]
	v_mfma_scale_f32_16x16x128_f8f6f4 v[122:125], v[26:33], v[238:245], v[122:125], v214, v214 op_sel_hi:[0,0,0]
	v_mfma_scale_f32_16x16x128_f8f6f4 v[118:121], v[18:25], v[246:253], v[118:121], v214, v214 op_sel_hi:[0,0,0]
	v_mfma_scale_f32_16x16x128_f8f6f4 v[114:117], v[26:33], v[246:253], v[114:117], v214, v214 op_sel_hi:[0,0,0]
	s_nop 3
	s_setprio 0
	s_setprio 1
	v_mfma_scale_f32_16x16x128_f8f6f4 v[110:113], v[2:9], v[222:229], v[110:113], v214, v214 op_sel_hi:[0,0,0]
	v_mfma_scale_f32_16x16x128_f8f6f4 v[106:109], v[10:17], v[222:229], v[106:109], v214, v214 op_sel_hi:[0,0,0]
	v_mfma_scale_f32_16x16x128_f8f6f4 v[102:105], v[2:9], v[230:237], v[102:105], v214, v214 op_sel_hi:[0,0,0]
	v_mfma_scale_f32_16x16x128_f8f6f4 v[98:101], v[10:17], v[230:237], v[98:101], v214, v214 op_sel_hi:[0,0,0]
	v_mfma_scale_f32_16x16x128_f8f6f4 v[94:97], v[2:9], v[238:245], v[94:97], v214, v214 op_sel_hi:[0,0,0]
	v_mfma_scale_f32_16x16x128_f8f6f4 v[90:93], v[10:17], v[238:245], v[90:93], v214, v214 op_sel_hi:[0,0,0]
	v_mfma_scale_f32_16x16x128_f8f6f4 v[86:89], v[2:9], v[246:253], v[86:89], v214, v214 op_sel_hi:[0,0,0]
	v_mfma_scale_f32_16x16x128_f8f6f4 v[82:85], v[10:17], v[246:253], v[82:85], v214, v214 op_sel_hi:[0,0,0]
	s_setprio 0
	s_barrier
	s_add_i32 s30, s12, s48
	v_lshl_add_u64 v[204:205], s[40:41], 0, v[162:163]
	s_mov_b32 m0, s30
	ds_read_b128 v[222:225], v213 offset:16384
	ds_read_b128 v[226:229], v213 offset:17408
	ds_read_b128 v[230:233], v213 offset:18432
	ds_read_b128 v[234:237], v213 offset:19456
	ds_read_b128 v[238:241], v213 offset:20480
	ds_read_b128 v[242:245], v213 offset:21504
	ds_read_b128 v[246:249], v213 offset:22528
	ds_read_b128 v[250:253], v213 offset:23552
	global_load_lds_dwordx4 v[204:205], off
	v_lshl_add_u64 v[204:205], s[40:41], 0, v[164:165]
	s_add_i32 m0, s30, 0x2000
	s_add_i32 s30, s62, s48
	global_load_lds_dwordx4 v[204:205], off
	v_lshl_add_u64 v[204:205], s[40:41], 0, v[166:167]
	s_mov_b32 m0, s30
	v_mov_b32_e32 v203, v171
	global_load_lds_dwordx4 v[204:205], off
	v_lshl_add_u64 v[204:205], s[40:41], 0, v[168:169]
	s_add_i32 m0, s30, 0x2000
	s_nop 0
	global_load_lds_dwordx4 v[204:205], off
	s_mov_b32 m0, s52
	v_lshl_add_u64 v[204:205], s[42:43], 0, v[170:171]
	global_load_lds_dwordx4 v170, s[42:43]
	s_mov_b32 m0, s53
	s_nop 0
	global_load_lds_dwordx4 v202, s[42:43]
	s_waitcnt vmcnt(8)
	s_waitcnt lgkmcnt(0)
	v_lshl_add_u64 v[202:203], s[42:43], 0, v[202:203]
	s_setprio 1
	v_mfma_scale_f32_16x16x128_f8f6f4 v[78:81], v[18:25], v[222:229], v[78:81], v214, v214 op_sel_hi:[0,0,0]
	v_mfma_scale_f32_16x16x128_f8f6f4 v[74:77], v[26:33], v[222:229], v[74:77], v214, v214 op_sel_hi:[0,0,0]
	v_mfma_scale_f32_16x16x128_f8f6f4 v[70:73], v[18:25], v[230:237], v[70:73], v214, v214 op_sel_hi:[0,0,0]
	v_mfma_scale_f32_16x16x128_f8f6f4 v[66:69], v[26:33], v[230:237], v[66:69], v214, v214 op_sel_hi:[0,0,0]
	v_mfma_scale_f32_16x16x128_f8f6f4 v[62:65], v[18:25], v[238:245], v[62:65], v214, v214 op_sel_hi:[0,0,0]
	v_mfma_scale_f32_16x16x128_f8f6f4 v[58:61], v[26:33], v[238:245], v[58:61], v214, v214 op_sel_hi:[0,0,0]
	v_mfma_scale_f32_16x16x128_f8f6f4 v[54:57], v[18:25], v[246:253], v[54:57], v214, v214 op_sel_hi:[0,0,0]
	v_mfma_scale_f32_16x16x128_f8f6f4 v[50:53], v[26:33], v[246:253], v[50:53], v214, v214 op_sel_hi:[0,0,0]
	s_nop 3
	s_setprio 0
	s_setprio 1
	v_mfma_scale_f32_16x16x128_f8f6f4 v[46:49], v[2:9], v[222:229], v[46:49], v214, v214 op_sel_hi:[0,0,0]
	v_mfma_scale_f32_16x16x128_f8f6f4 v[42:45], v[10:17], v[222:229], v[42:45], v214, v214 op_sel_hi:[0,0,0]
	v_mfma_scale_f32_16x16x128_f8f6f4 v[38:41], v[2:9], v[230:237], v[38:41], v214, v214 op_sel_hi:[0,0,0]
	v_mfma_scale_f32_16x16x128_f8f6f4 v[34:37], v[10:17], v[230:237], v[34:37], v214, v214 op_sel_hi:[0,0,0]
	v_mfma_scale_f32_16x16x128_f8f6f4 v[146:149], v[2:9], v[238:245], v[146:149], v214, v214 op_sel_hi:[0,0,0]
	v_mfma_scale_f32_16x16x128_f8f6f4 v[150:153], v[10:17], v[238:245], v[150:153], v214, v214 op_sel_hi:[0,0,0]
	v_mfma_scale_f32_16x16x128_f8f6f4 v[154:157], v[2:9], v[246:253], v[154:157], v214, v214 op_sel_hi:[0,0,0]
	v_mfma_scale_f32_16x16x128_f8f6f4 v[158:161], v[10:17], v[246:253], v[158:161], v214, v214 op_sel_hi:[0,0,0]
	s_setprio 0
	s_barrier
; #define PG8_STAGE(bufoff, gbase, voff) do { _Pragma("unroll") for (int _i = 0; _i < 2; ++_i) \
;         __builtin_amdgcn_global_load_lds((const unsigned*)((const char*)(gbase) + (voff)[_i]), (PG8_LAS unsigned*)(lds + (bufoff) + ldsw + _i * 8192), 16, 0, 0); } while (0)
; #define PG8_WAIT_V(n) asm volatile("s_waitcnt vmcnt(" #n ")" ::: "memory")
; #define PG8_WAIT_L(n) asm volatile("s_waitcnt lgkmcnt(" #n ")" ::: "memory")
; #define PG8_BAR __builtin_amdgcn_s_barrier()
; #define PG8_SCHED __builtin_amdgcn_sched_barrier(0)
; template <class Epi, class Sched, bool ALIGN_EPI = true, bool F8 = false>
; __device__ __forceinline__ void gemm_phase(PG8_LAS unsigned char* lds, const Sched& S, const Epi& E) {
;     ...
;             PG8_LDB(B0, 1, 0); PG8_LDB(B1, 1, 1); PG8_SCHED; PG8_LDA(At, 1, 0); PG8_STAGE(PG8_SA(0, 1), a2, vA2[1]);
;             PG8_WAIT_V(8); PG8_WAIT_L(0); PG8_BAR; PG8_MMA(0, 0, At, B0); PG8_MMA(0, 1, At, B1); PG8_BAR; PG8_SCHED;
;             PG8_LDA(At, 1, 1); PG8_STAGE(PG8_SB(1, 0), b3, voffB[0]); PG8_STAGE(PG8_SB(1, 1), b3, voffB[1]); PG8_STAGE(PG8_SA(1, 0), a3, vA2[0]);
;             PG8_WAIT_V(8); PG8_WAIT_L(0); PG8_BAR; PG8_MMA(1, 0, At, B0); PG8_MMA(1, 1, At, B1); PG8_BAR; PG8_SCHED;
	s_add_i32 s70, 0, 0x18000
	s_add_i32 s71, 0, 0x1c000
	v_add_u32_e32 v14, s70, v210
	v_add_u32_e32 v30, s71, v210
	ds_read_b128 v[2:5], v14
	ds_read_b128 v[6:9], v14 offset:1024
	ds_read_b128 v[10:13], v14 offset:2048
	ds_read_b128 v[14:17], v14 offset:3072
	ds_read_b128 v[18:21], v30
	ds_read_b128 v[22:25], v30 offset:1024
	ds_read_b128 v[26:29], v30 offset:2048
	ds_read_b128 v[30:33], v30 offset:3072
	s_mov_b32 m0, s58
	v_lshl_add_u64 v[200:201], s[42:43], 0, v[200:201]
	ds_read_b128 v[222:225], v213 offset:32768
	ds_read_b128 v[226:229], v213 offset:33792
	ds_read_b128 v[230:233], v213 offset:34816
	ds_read_b128 v[234:237], v213 offset:35840
	ds_read_b128 v[238:241], v213 offset:36864
	ds_read_b128 v[242:245], v213 offset:37888
	ds_read_b128 v[246:249], v213 offset:38912
	ds_read_b128 v[250:253], v213 offset:39936
	global_load_lds_dwordx4 v[200:201], off
	v_lshl_add_u64 v[198:199], s[42:43], 0, v[198:199]
	s_mov_b32 m0, s59
	s_nop 0
	global_load_lds_dwordx4 v[198:199], off
	s_waitcnt vmcnt(8)
	s_waitcnt lgkmcnt(0)
	s_setprio 1
	v_mfma_scale_f32_16x16x128_f8f6f4 v[142:145], v[2:9], v[222:229], v[142:145], v214, v214 op_sel_hi:[0,0,0]
	v_mfma_scale_f32_16x16x128_f8f6f4 v[138:141], v[10:17], v[222:229], v[138:141], v214, v214 op_sel_hi:[0,0,0]
	v_mfma_scale_f32_16x16x128_f8f6f4 v[134:137], v[2:9], v[230:237], v[134:137], v214, v214 op_sel_hi:[0,0,0]
	v_mfma_scale_f32_16x16x128_f8f6f4 v[130:133], v[10:17], v[230:237], v[130:133], v214, v214 op_sel_hi:[0,0,0]
	v_mfma_scale_f32_16x16x128_f8f6f4 v[126:129], v[2:9], v[238:245], v[126:129], v214, v214 op_sel_hi:[0,0,0]
	v_mfma_scale_f32_16x16x128_f8f6f4 v[122:125], v[10:17], v[238:245], v[122:125], v214, v214 op_sel_hi:[0,0,0]
	v_mfma_scale_f32_16x16x128_f8f6f4 v[118:121], v[2:9], v[246:253], v[118:121], v214, v214 op_sel_hi:[0,0,0]
	v_mfma_scale_f32_16x16x128_f8f6f4 v[114:117], v[10:17], v[246:253], v[114:117], v214, v214 op_sel_hi:[0,0,0]
	s_nop 3
	s_setprio 0
	s_setprio 1
	v_mfma_scale_f32_16x16x128_f8f6f4 v[110:113], v[18:25], v[222:229], v[110:113], v214, v214 op_sel_hi:[0,0,0]
	v_mfma_scale_f32_16x16x128_f8f6f4 v[106:109], v[26:33], v[222:229], v[106:109], v214, v214 op_sel_hi:[0,0,0]
	v_mfma_scale_f32_16x16x128_f8f6f4 v[102:105], v[18:25], v[230:237], v[102:105], v214, v214 op_sel_hi:[0,0,0]
	v_mfma_scale_f32_16x16x128_f8f6f4 v[98:101], v[26:33], v[230:237], v[98:101], v214, v214 op_sel_hi:[0,0,0]
	v_mfma_scale_f32_16x16x128_f8f6f4 v[94:97], v[18:25], v[238:245], v[94:97], v214, v214 op_sel_hi:[0,0,0]
	v_mfma_scale_f32_16x16x128_f8f6f4 v[90:93], v[26:33], v[238:245], v[90:93], v214, v214 op_sel_hi:[0,0,0]
	v_mfma_scale_f32_16x16x128_f8f6f4 v[86:89], v[18:25], v[246:253], v[86:89], v214, v214 op_sel_hi:[0,0,0]
	v_mfma_scale_f32_16x16x128_f8f6f4 v[82:85], v[26:33], v[246:253], v[82:85], v214, v214 op_sel_hi:[0,0,0]
	s_setprio 0
	s_barrier
	s_add_u32 s30, s40, 0x8000
	s_addc_u32 s31, s41, 0
	s_add_i32 s40, s70, s48
	v_lshl_add_u64 v[198:199], s[30:31], 0, v[162:163]
	s_mov_b32 m0, s40
	ds_read_b128 v[222:225], v213 offset:49152
	ds_read_b128 v[226:229], v213 offset:50176
	ds_read_b128 v[230:233], v213 offset:51200
	ds_read_b128 v[234:237], v213 offset:52224
	ds_read_b128 v[238:241], v213 offset:53248
	ds_read_b128 v[242:245], v213 offset:54272
	ds_read_b128 v[246:249], v213 offset:55296
	ds_read_b128 v[250:253], v213 offset:56320
	global_load_lds_dwordx4 v[198:199], off
	v_lshl_add_u64 v[198:199], s[30:31], 0, v[164:165]
	s_add_i32 m0, s40, 0x2000
	s_add_i32 s40, s71, s48
	global_load_lds_dwordx4 v[198:199], off
	v_lshl_add_u64 v[198:199], s[30:31], 0, v[166:167]
	s_mov_b32 m0, s40
	s_nop 0
	global_load_lds_dwordx4 v[198:199], off
	v_lshl_add_u64 v[198:199], s[30:31], 0, v[168:169]
	s_add_i32 m0, s40, 0x2000
	s_nop 0
	global_load_lds_dwordx4 v[198:199], off
	v_lshl_add_u64 v[198:199], v[204:205], 0, s[18:19]
	s_mov_b32 m0, s60
	s_nop 0
	global_load_lds_dwordx4 v[198:199], off
	v_lshl_add_u64 v[198:199], v[202:203], 0, s[18:19]
	s_mov_b32 m0, s61
	s_nop 0
	global_load_lds_dwordx4 v[198:199], off
	s_waitcnt vmcnt(8)
	s_waitcnt lgkmcnt(0)
	s_setprio 1
	v_mfma_scale_f32_16x16x128_f8f6f4 v[78:81], v[2:9], v[222:229], v[78:81], v214, v214 op_sel_hi:[0,0,0]
	v_mfma_scale_f32_16x16x128_f8f6f4 v[74:77], v[10:17], v[222:229], v[74:77], v214, v214 op_sel_hi:[0,0,0]
	v_mfma_scale_f32_16x16x128_f8f6f4 v[70:73], v[2:9], v[230:237], v[70:73], v214, v214 op_sel_hi:[0,0,0]
	v_mfma_scale_f32_16x16x128_f8f6f4 v[66:69], v[10:17], v[230:237], v[66:69], v214, v214 op_sel_hi:[0,0,0]
	v_mfma_scale_f32_16x16x128_f8f6f4 v[62:65], v[2:9], v[238:245], v[62:65], v214, v214 op_sel_hi:[0,0,0]
	v_mfma_scale_f32_16x16x128_f8f6f4 v[58:61], v[10:17], v[238:245], v[58:61], v214, v214 op_sel_hi:[0,0,0]
	v_mfma_scale_f32_16x16x128_f8f6f4 v[54:57], v[2:9], v[246:253], v[54:57], v214, v214 op_sel_hi:[0,0,0]
	v_mfma_scale_f32_16x16x128_f8f6f4 v[50:53], v[10:17], v[246:253], v[50:53], v214, v214 op_sel_hi:[0,0,0]
	s_nop 3
	s_setprio 0
	s_setprio 1
	v_mfma_scale_f32_16x16x128_f8f6f4 v[46:49], v[18:25], v[222:229], v[46:49], v214, v214 op_sel_hi:[0,0,0]
	v_mfma_scale_f32_16x16x128_f8f6f4 v[42:45], v[26:33], v[222:229], v[42:45], v214, v214 op_sel_hi:[0,0,0]
	v_mfma_scale_f32_16x16x128_f8f6f4 v[38:41], v[18:25], v[230:237], v[38:41], v214, v214 op_sel_hi:[0,0,0]
	v_mfma_scale_f32_16x16x128_f8f6f4 v[34:37], v[26:33], v[230:237], v[34:37], v214, v214 op_sel_hi:[0,0,0]
	v_mfma_scale_f32_16x16x128_f8f6f4 v[146:149], v[18:25], v[238:245], v[146:149], v214, v214 op_sel_hi:[0,0,0]
	v_mfma_scale_f32_16x16x128_f8f6f4 v[150:153], v[26:33], v[238:245], v[150:153], v214, v214 op_sel_hi:[0,0,0]
	v_mfma_scale_f32_16x16x128_f8f6f4 v[154:157], v[18:25], v[246:253], v[154:157], v214, v214 op_sel_hi:[0,0,0]
	v_mfma_scale_f32_16x16x128_f8f6f4 v[158:161], v[26:33], v[246:253], v[158:161], v214, v214 op_sel_hi:[0,0,0]
	s_setprio 0
	s_barrier
	s_add_i32 s69, s69, 2
	s_add_u32 s21, s21, 0x10000
	s_addc_u32 s68, s68, 0
	s_cmp_gt_u32 s69, 13
	s_cbranch_scc1 .LBB0_1062
	s_mov_b64 s[30:31], s[28:29]
	s_branch .LBB0_1058
	.p2align	6

; #define PG8_STAGE(bufoff, gbase, voff) do { _Pragma("unroll") for (int _i = 0; _i < 2; ++_i) \
;         __builtin_amdgcn_global_load_lds((const unsigned*)((const char*)(gbase) + (voff)[_i]), (PG8_LAS unsigned*)(lds + (bufoff) + ldsw + _i * 8192), 16, 0, 0); } while (0)
; #define PG8_WAIT_V(n) asm volatile("s_waitcnt vmcnt(" #n ")" ::: "memory")
; #define PG8_WAIT_L(n) asm volatile("s_waitcnt lgkmcnt(" #n ")" ::: "memory")
; #define PG8_BAR __builtin_amdgcn_s_barrier()
; #define PG8_SCHED __builtin_amdgcn_sched_barrier(0)
; template <class Epi, class Sched, bool ALIGN_EPI = true, bool F8 = false>
; __device__ __forceinline__ void gemm_phase(PG8_LAS unsigned char* lds, const Sched& S, const Epi& E) {
;     ...
;             PG8_LDB(B0, 0, 0); PG8_LDB(B1, 0, 1); PG8_SCHED; PG8_LDA(At, 0, 0); PG8_STAGE(PG8_SA(1, 1), a1, voffA[1]);
;             PG8_WAIT_V(8); PG8_WAIT_L(0); PG8_BAR; PG8_MMA(0, 0, At, B0); PG8_MMA(0, 1, At, B1); PG8_BAR; PG8_SCHED;
;             PG8_LDA(At, 0, 1); PG8_STAGE(PG8_SB(0, 0), b2, voffB[0]); PG8_STAGE(PG8_SB(0, 1), b2, voffB[1]); PG8_STAGE(PG8_SA(0, 0), a2, vA2[0]);
;             PG8_WAIT_V(8); PG8_WAIT_L(0); PG8_BAR; PG8_MMA(1, 0, At, B0); PG8_MMA(1, 1, At, B1); PG8_BAR; PG8_SCHED;
;     ...
; #pragma unroll
;         for (int a = 0; a < 2; ++a)
; #pragma unroll
;             for (int b = 0; b < 2; ++b)
; #pragma unroll
;                 for (int m = 0; m < 4; ++m)
; #pragma unroll
;                     for (int n = 0; n < 2; ++n) acc[a][b][m][n] = (f32x4){0.f, 0.f, 0.f, 0.f};
;         }
;         cur = nxt; cA = nA; cB = nB; ++ui;
; #pragma unroll
;         for (int h = 0; h < 2; ++h)
; #pragma unroll
;             for (int i = 0; i < 2; ++i) voffA[h][i] = voffAn[h][i];
.LBB0_1137:
	s_add_u32 s23, s26, 0x10000
	s_addc_u32 s67, s27, 0
	s_add_u32 s24, s24, 0x8000
	v_mov_b64_e32 v[34:35], 0
	s_addc_u32 s25, s25, 0
	s_mov_b32 s68, -2
	v_mov_b64_e32 v[36:37], 0
	v_mov_b64_e32 v[38:39], 0
	v_mov_b64_e32 v[40:41], 0
	v_mov_b64_e32 v[50:51], 0
	v_mov_b64_e32 v[52:53], 0
	v_mov_b64_e32 v[54:55], 0
	v_mov_b64_e32 v[56:57], 0
	v_mov_b64_e32 v[66:67], 0
	v_mov_b64_e32 v[68:69], 0
	v_mov_b64_e32 v[70:71], 0
	v_mov_b64_e32 v[72:73], 0
	v_mov_b64_e32 v[82:83], 0
	v_mov_b64_e32 v[84:85], 0
	v_mov_b64_e32 v[86:87], 0
	v_mov_b64_e32 v[88:89], 0
	v_mov_b64_e32 v[42:43], 0
	v_mov_b64_e32 v[44:45], 0
	v_mov_b64_e32 v[46:47], 0
	v_mov_b64_e32 v[48:49], 0
	v_mov_b64_e32 v[58:59], 0
	v_mov_b64_e32 v[60:61], 0
	v_mov_b64_e32 v[62:63], 0
	v_mov_b64_e32 v[64:65], 0
	v_mov_b64_e32 v[74:75], 0
	v_mov_b64_e32 v[76:77], 0
	v_mov_b64_e32 v[78:79], 0
	v_mov_b64_e32 v[80:81], 0
	v_mov_b64_e32 v[90:91], 0
	v_mov_b64_e32 v[92:93], 0
	v_mov_b64_e32 v[94:95], 0
	v_mov_b64_e32 v[96:97], 0
	v_mov_b64_e32 v[98:99], 0
	v_mov_b64_e32 v[100:101], 0
	v_mov_b64_e32 v[102:103], 0
	v_mov_b64_e32 v[104:105], 0
	v_mov_b64_e32 v[114:115], 0
	v_mov_b64_e32 v[116:117], 0
	v_mov_b64_e32 v[118:119], 0
	v_mov_b64_e32 v[120:121], 0
	v_mov_b64_e32 v[130:131], 0
	v_mov_b64_e32 v[132:133], 0
	v_mov_b64_e32 v[134:135], 0
	v_mov_b64_e32 v[136:137], 0
	v_mov_b64_e32 v[146:147], 0
	v_mov_b64_e32 v[148:149], 0
	v_mov_b64_e32 v[150:151], 0
	v_mov_b64_e32 v[152:153], 0
	v_mov_b64_e32 v[106:107], 0
	v_mov_b64_e32 v[108:109], 0
	v_mov_b64_e32 v[110:111], 0
	v_mov_b64_e32 v[112:113], 0
	v_mov_b64_e32 v[122:123], 0
	v_mov_b64_e32 v[124:125], 0
	v_mov_b64_e32 v[126:127], 0
	v_mov_b64_e32 v[128:129], 0
	v_mov_b64_e32 v[138:139], 0
	v_mov_b64_e32 v[140:141], 0
	v_mov_b64_e32 v[142:143], 0
	v_mov_b64_e32 v[144:145], 0
	v_mov_b64_e32 v[154:155], 0
	v_mov_b64_e32 v[156:157], 0
	v_mov_b64_e32 v[158:159], 0
	v_mov_b64_e32 v[160:161], 0
	s_bitcmp1_b32 s3, 2
	s_cbranch_scc1 .Lh1e_33571
	.p2align	6
.LBB0_1138:
	ds_read_b128 v[18:21], v189
	ds_read_b128 v[22:25], v189 offset:1024
	ds_read_b128 v[26:29], v189 offset:2048
	ds_read_b128 v[30:33], v189 offset:3072
	ds_read_b128 v[2:5], v190
	ds_read_b128 v[6:9], v190 offset:1024
	ds_read_b128 v[10:13], v190 offset:2048
	ds_read_b128 v[14:17], v190 offset:3072
	s_add_u32 s26, s24, 0x8000
	s_addc_u32 s27, s25, 0
	s_cmp_eq_u32 s68, 4
	s_cselect_b32 s30, s16, s26
	s_cselect_b32 s31, s17, s27
	s_cselect_b32 s28, s18, s23
	s_cselect_b32 s29, s19, s67
	s_add_u32 s26, s30, 0x8000
	s_addc_u32 s27, s31, 0
	v_lshl_add_u64 v[226:227], s[24:25], 0, v[184:185]
	s_add_i32 m0, s44, 0xc000
	ds_read_b128 v[194:197], v191
	ds_read_b128 v[198:201], v191 offset:1024
	ds_read_b128 v[202:205], v191 offset:2048
	ds_read_b128 v[206:209], v191 offset:3072
	ds_read_b128 v[210:213], v191 offset:4096
	ds_read_b128 v[214:217], v191 offset:5120
	ds_read_b128 v[218:221], v191 offset:6144
	ds_read_b128 v[222:225], v191 offset:7168
	global_load_lds_dwordx4 v[226:227], off
	v_lshl_add_u64 v[226:227], s[24:25], 0, v[182:183]
	s_add_i32 m0, s44, 0xe000
	s_nop 0
	global_load_lds_dwordx4 v[226:227], off
	s_waitcnt vmcnt(8)
	s_waitcnt lgkmcnt(0)
	s_setprio 1
	v_mfma_scale_f32_16x16x128_f8f6f4 v[158:161], v[18:25], v[194:201], v[158:161], v192, v192 op_sel_hi:[0,0,0]
	v_mfma_scale_f32_16x16x128_f8f6f4 v[154:157], v[26:33], v[194:201], v[154:157], v192, v192 op_sel_hi:[0,0,0]
	v_mfma_scale_f32_16x16x128_f8f6f4 v[142:145], v[18:25], v[202:209], v[142:145], v192, v192 op_sel_hi:[0,0,0]
	v_mfma_scale_f32_16x16x128_f8f6f4 v[138:141], v[26:33], v[202:209], v[138:141], v192, v192 op_sel_hi:[0,0,0]
	v_mfma_scale_f32_16x16x128_f8f6f4 v[126:129], v[18:25], v[210:217], v[126:129], v192, v192 op_sel_hi:[0,0,0]
	v_mfma_scale_f32_16x16x128_f8f6f4 v[122:125], v[26:33], v[210:217], v[122:125], v192, v192 op_sel_hi:[0,0,0]
	v_mfma_scale_f32_16x16x128_f8f6f4 v[110:113], v[18:25], v[218:225], v[110:113], v192, v192 op_sel_hi:[0,0,0]
	v_mfma_scale_f32_16x16x128_f8f6f4 v[106:109], v[26:33], v[218:225], v[106:109], v192, v192 op_sel_hi:[0,0,0]
	s_nop 3
	s_setprio 0
	s_setprio 1
	v_mfma_scale_f32_16x16x128_f8f6f4 v[150:153], v[2:9], v[194:201], v[150:153], v192, v192 op_sel_hi:[0,0,0]
	v_mfma_scale_f32_16x16x128_f8f6f4 v[146:149], v[10:17], v[194:201], v[146:149], v192, v192 op_sel_hi:[0,0,0]
	v_mfma_scale_f32_16x16x128_f8f6f4 v[134:137], v[2:9], v[202:209], v[134:137], v192, v192 op_sel_hi:[0,0,0]
	v_mfma_scale_f32_16x16x128_f8f6f4 v[130:133], v[10:17], v[202:209], v[130:133], v192, v192 op_sel_hi:[0,0,0]
	v_mfma_scale_f32_16x16x128_f8f6f4 v[118:121], v[2:9], v[210:217], v[118:121], v192, v192 op_sel_hi:[0,0,0]
	v_mfma_scale_f32_16x16x128_f8f6f4 v[114:117], v[10:17], v[210:217], v[114:117], v192, v192 op_sel_hi:[0,0,0]
	v_mfma_scale_f32_16x16x128_f8f6f4 v[102:105], v[2:9], v[218:225], v[102:105], v192, v192 op_sel_hi:[0,0,0]
	v_mfma_scale_f32_16x16x128_f8f6f4 v[98:101], v[10:17], v[218:225], v[98:101], v192, v192 op_sel_hi:[0,0,0]
	s_setprio 0
	s_barrier
; #define PG8_STAGE(bufoff, gbase, voff) do { _Pragma("unroll") for (int _i = 0; _i < 2; ++_i) \
;         __builtin_amdgcn_global_load_lds((const unsigned*)((const char*)(gbase) + (voff)[_i]), (PG8_LAS unsigned*)(lds + (bufoff) + ldsw + _i * 8192), 16, 0, 0); } while (0)
; #define PG8_WAIT_V(n) asm volatile("s_waitcnt vmcnt(" #n ")" ::: "memory")
; #define PG8_WAIT_L(n) asm volatile("s_waitcnt lgkmcnt(" #n ")" ::: "memory")
; #define PG8_BAR __builtin_amdgcn_s_barrier()
; #define PG8_SCHED __builtin_amdgcn_sched_barrier(0)
; template <class Epi, class Sched, bool ALIGN_EPI = true, bool F8 = false>
; __device__ __forceinline__ void gemm_phase(PG8_LAS unsigned char* lds, const Sched& S, const Epi& E) {
;     ...
;             PG8_LDA(At, 0, 1); PG8_STAGE(PG8_SB(0, 0), b2, voffB[0]); PG8_STAGE(PG8_SB(0, 1), b2, voffB[1]); PG8_STAGE(PG8_SA(0, 0), a2, vA2[0]);
;             PG8_WAIT_V(8); PG8_WAIT_L(0); PG8_BAR; PG8_MMA(1, 0, At, B0); PG8_MMA(1, 1, At, B1); PG8_BAR; PG8_SCHED;
;             PG8_LDB(B0, 1, 0); PG8_LDB(B1, 1, 1); PG8_SCHED; PG8_LDA(At, 1, 0); PG8_STAGE(PG8_SA(0, 1), a2, vA2[1]);
;             PG8_WAIT_V(8); PG8_WAIT_L(0); PG8_BAR; PG8_MMA(0, 0, At, B0); PG8_MMA(0, 1, At, B1); PG8_BAR; PG8_SCHED;
	s_add_i32 s69, s53, s43
	v_lshl_add_u64 v[226:227], s[28:29], 0, v[164:165]
	s_mov_b32 m0, s69
	ds_read_b128 v[194:197], v191 offset:16384
	ds_read_b128 v[198:201], v191 offset:17408
	ds_read_b128 v[202:205], v191 offset:18432
	ds_read_b128 v[206:209], v191 offset:19456
	ds_read_b128 v[210:213], v191 offset:20480
	ds_read_b128 v[214:217], v191 offset:21504
	ds_read_b128 v[218:221], v191 offset:22528
	ds_read_b128 v[222:225], v191 offset:23552
	global_load_lds_dwordx4 v[226:227], off
	v_lshl_add_u64 v[228:229], s[28:29], 0, v[166:167]
	s_add_i32 m0, s69, 0x2000
	s_add_i32 s69, s58, s43
	global_load_lds_dwordx4 v[228:229], off
	v_lshl_add_u64 v[226:227], v[226:227], 0, s[4:5]
	s_mov_b32 m0, s69
	s_nop 0
	global_load_lds_dwordx4 v[226:227], off
	v_lshl_add_u64 v[226:227], v[228:229], 0, s[4:5]
	s_add_i32 m0, s69, 0x2000
	s_nop 0
	global_load_lds_dwordx4 v[226:227], off
	v_lshl_add_u64 v[226:227], s[30:31], 0, v[168:169]
	s_mov_b32 m0, s44
	s_nop 0
	global_load_lds_dwordx4 v[226:227], off
	v_lshl_add_u64 v[226:227], s[30:31], 0, v[170:171]
	s_mov_b32 m0, s45
	s_nop 0
	global_load_lds_dwordx4 v[226:227], off
	s_waitcnt vmcnt(8)
	s_waitcnt lgkmcnt(0)
	s_setprio 1
	v_mfma_scale_f32_16x16x128_f8f6f4 v[94:97], v[18:25], v[194:201], v[94:97], v192, v192 op_sel_hi:[0,0,0]
	v_mfma_scale_f32_16x16x128_f8f6f4 v[90:93], v[26:33], v[194:201], v[90:93], v192, v192 op_sel_hi:[0,0,0]
	v_mfma_scale_f32_16x16x128_f8f6f4 v[78:81], v[18:25], v[202:209], v[78:81], v192, v192 op_sel_hi:[0,0,0]
	v_mfma_scale_f32_16x16x128_f8f6f4 v[74:77], v[26:33], v[202:209], v[74:77], v192, v192 op_sel_hi:[0,0,0]
	v_mfma_scale_f32_16x16x128_f8f6f4 v[62:65], v[18:25], v[210:217], v[62:65], v192, v192 op_sel_hi:[0,0,0]
	v_mfma_scale_f32_16x16x128_f8f6f4 v[58:61], v[26:33], v[210:217], v[58:61], v192, v192 op_sel_hi:[0,0,0]
	v_mfma_scale_f32_16x16x128_f8f6f4 v[46:49], v[18:25], v[218:225], v[46:49], v192, v192 op_sel_hi:[0,0,0]
	v_mfma_scale_f32_16x16x128_f8f6f4 v[42:45], v[26:33], v[218:225], v[42:45], v192, v192 op_sel_hi:[0,0,0]
	s_nop 3
	s_setprio 0
	s_setprio 1
	v_mfma_scale_f32_16x16x128_f8f6f4 v[86:89], v[2:9], v[194:201], v[86:89], v192, v192 op_sel_hi:[0,0,0]
	v_mfma_scale_f32_16x16x128_f8f6f4 v[82:85], v[10:17], v[194:201], v[82:85], v192, v192 op_sel_hi:[0,0,0]
	v_mfma_scale_f32_16x16x128_f8f6f4 v[70:73], v[2:9], v[202:209], v[70:73], v192, v192 op_sel_hi:[0,0,0]
	v_mfma_scale_f32_16x16x128_f8f6f4 v[66:69], v[10:17], v[202:209], v[66:69], v192, v192 op_sel_hi:[0,0,0]
	v_mfma_scale_f32_16x16x128_f8f6f4 v[54:57], v[2:9], v[210:217], v[54:57], v192, v192 op_sel_hi:[0,0,0]
	v_mfma_scale_f32_16x16x128_f8f6f4 v[50:53], v[10:17], v[210:217], v[50:53], v192, v192 op_sel_hi:[0,0,0]
	v_mfma_scale_f32_16x16x128_f8f6f4 v[38:41], v[2:9], v[218:225], v[38:41], v192, v192 op_sel_hi:[0,0,0]
	v_mfma_scale_f32_16x16x128_f8f6f4 v[34:37], v[10:17], v[218:225], v[34:37], v192, v192 op_sel_hi:[0,0,0]
	s_setprio 0
	s_barrier
	s_add_i32 s69, 0, 0x18000
	s_add_i32 s70, 0, 0x1c000
	v_add_u32_e32 v14, s69, v187
	v_add_u32_e32 v30, s70, v187
	ds_read_b128 v[2:5], v14
	ds_read_b128 v[6:9], v14 offset:1024
	ds_read_b128 v[10:13], v14 offset:2048
	ds_read_b128 v[14:17], v14 offset:3072
	ds_read_b128 v[18:21], v30
	ds_read_b128 v[22:25], v30 offset:1024
	ds_read_b128 v[26:29], v30 offset:2048
	ds_read_b128 v[30:33], v30 offset:3072
	s_mov_b32 m0, s46
	v_lshl_add_u64 v[226:227], s[30:31], 0, v[172:173]
	ds_read_b128 v[194:197], v191 offset:32768
	ds_read_b128 v[198:201], v191 offset:33792
	ds_read_b128 v[202:205], v191 offset:34816
	ds_read_b128 v[206:209], v191 offset:35840
	ds_read_b128 v[210:213], v191 offset:36864
	ds_read_b128 v[214:217], v191 offset:37888
	ds_read_b128 v[218:221], v191 offset:38912
	ds_read_b128 v[222:225], v191 offset:39936
	global_load_lds_dwordx4 v[226:227], off
	v_lshl_add_u64 v[226:227], s[30:31], 0, v[174:175]
	s_mov_b32 m0, s47
	s_nop 0
	global_load_lds_dwordx4 v[226:227], off
	s_waitcnt vmcnt(8)
	s_waitcnt lgkmcnt(0)
	s_setprio 1
	v_mfma_scale_f32_16x16x128_f8f6f4 v[158:161], v[2:9], v[194:201], v[158:161], v192, v192 op_sel_hi:[0,0,0]
	v_mfma_scale_f32_16x16x128_f8f6f4 v[154:157], v[10:17], v[194:201], v[154:157], v192, v192 op_sel_hi:[0,0,0]
	v_mfma_scale_f32_16x16x128_f8f6f4 v[142:145], v[2:9], v[202:209], v[142:145], v192, v192 op_sel_hi:[0,0,0]
	v_mfma_scale_f32_16x16x128_f8f6f4 v[138:141], v[10:17], v[202:209], v[138:141], v192, v192 op_sel_hi:[0,0,0]
	v_mfma_scale_f32_16x16x128_f8f6f4 v[126:129], v[2:9], v[210:217], v[126:129], v192, v192 op_sel_hi:[0,0,0]
	v_mfma_scale_f32_16x16x128_f8f6f4 v[122:125], v[10:17], v[210:217], v[122:125], v192, v192 op_sel_hi:[0,0,0]
	v_mfma_scale_f32_16x16x128_f8f6f4 v[110:113], v[2:9], v[218:225], v[110:113], v192, v192 op_sel_hi:[0,0,0]
	v_mfma_scale_f32_16x16x128_f8f6f4 v[106:109], v[10:17], v[218:225], v[106:109], v192, v192 op_sel_hi:[0,0,0]
	s_nop 3
	s_setprio 0
	s_setprio 1
	v_mfma_scale_f32_16x16x128_f8f6f4 v[150:153], v[18:25], v[194:201], v[150:153], v192, v192 op_sel_hi:[0,0,0]
	v_mfma_scale_f32_16x16x128_f8f6f4 v[146:149], v[26:33], v[194:201], v[146:149], v192, v192 op_sel_hi:[0,0,0]
	v_mfma_scale_f32_16x16x128_f8f6f4 v[134:137], v[18:25], v[202:209], v[134:137], v192, v192 op_sel_hi:[0,0,0]
	v_mfma_scale_f32_16x16x128_f8f6f4 v[130:133], v[26:33], v[202:209], v[130:133], v192, v192 op_sel_hi:[0,0,0]
	v_mfma_scale_f32_16x16x128_f8f6f4 v[118:121], v[18:25], v[210:217], v[118:121], v192, v192 op_sel_hi:[0,0,0]
	v_mfma_scale_f32_16x16x128_f8f6f4 v[114:117], v[26:33], v[210:217], v[114:117], v192, v192 op_sel_hi:[0,0,0]
	v_mfma_scale_f32_16x16x128_f8f6f4 v[102:105], v[18:25], v[218:225], v[102:105], v192, v192 op_sel_hi:[0,0,0]
	v_mfma_scale_f32_16x16x128_f8f6f4 v[98:101], v[26:33], v[218:225], v[98:101], v192, v192 op_sel_hi:[0,0,0]
	s_setprio 0
	s_barrier
; #define PG8_STAGE(bufoff, gbase, voff) do { _Pragma("unroll") for (int _i = 0; _i < 2; ++_i) \
;         __builtin_amdgcn_global_load_lds((const unsigned*)((const char*)(gbase) + (voff)[_i]), (PG8_LAS unsigned*)(lds + (bufoff) + ldsw + _i * 8192), 16, 0, 0); } while (0)
; #define PG8_WAIT_V(n) asm volatile("s_waitcnt vmcnt(" #n ")" ::: "memory")
; #define PG8_WAIT_L(n) asm volatile("s_waitcnt lgkmcnt(" #n ")" ::: "memory")
; #define PG8_BAR __builtin_amdgcn_s_barrier()
; #define PG8_SCHED __builtin_amdgcn_sched_barrier(0)
; template <class Epi, class Sched, bool ALIGN_EPI = true, bool F8 = false>
; __device__ __forceinline__ void gemm_phase(PG8_LAS unsigned char* lds, const Sched& S, const Epi& E) {
;     ...
;             PG8_LDA(At, 1, 1); PG8_STAGE(PG8_SB(1, 0), b3, voffB[0]); PG8_STAGE(PG8_SB(1, 1), b3, voffB[1]); PG8_STAGE(PG8_SA(1, 0), a3, vA2[0]);
;             PG8_WAIT_V(8); PG8_WAIT_L(0); PG8_BAR; PG8_MMA(1, 0, At, B0); PG8_MMA(1, 1, At, B1); PG8_BAR; PG8_SCHED;
	s_add_u32 s28, s28, 0x8000
	s_addc_u32 s29, s29, 0
	s_add_i32 s30, s69, s43
	v_lshl_add_u64 v[226:227], s[28:29], 0, v[164:165]
	s_mov_b32 m0, s30
	ds_read_b128 v[194:197], v191 offset:49152
	ds_read_b128 v[198:201], v191 offset:50176
	ds_read_b128 v[202:205], v191 offset:51200
	ds_read_b128 v[206:209], v191 offset:52224
	ds_read_b128 v[210:213], v191 offset:53248
	ds_read_b128 v[214:217], v191 offset:54272
	ds_read_b128 v[218:221], v191 offset:55296
	ds_read_b128 v[222:225], v191 offset:56320
	global_load_lds_dwordx4 v[226:227], off
	v_lshl_add_u64 v[226:227], s[28:29], 0, v[166:167]
	s_add_i32 m0, s30, 0x2000
	s_add_i32 s30, s70, s43
	global_load_lds_dwordx4 v[226:227], off
	v_lshl_add_u64 v[226:227], s[28:29], 0, v[178:179]
	s_mov_b32 m0, s30
	s_nop 0
	global_load_lds_dwordx4 v[226:227], off
	v_lshl_add_u64 v[226:227], s[28:29], 0, v[180:181]
	s_add_i32 m0, s30, 0x2000
	s_nop 0
	global_load_lds_dwordx4 v[226:227], off
	v_lshl_add_u64 v[226:227], s[26:27], 0, v[168:169]
	s_mov_b32 m0, s51
	s_nop 0
	global_load_lds_dwordx4 v[226:227], off
	v_lshl_add_u64 v[226:227], s[26:27], 0, v[170:171]
	s_mov_b32 m0, s52
	s_nop 0
	global_load_lds_dwordx4 v[226:227], off
	s_waitcnt vmcnt(8)
	s_waitcnt lgkmcnt(0)
	s_setprio 1
	v_mfma_scale_f32_16x16x128_f8f6f4 v[94:97], v[2:9], v[194:201], v[94:97], v192, v192 op_sel_hi:[0,0,0]
	v_mfma_scale_f32_16x16x128_f8f6f4 v[90:93], v[10:17], v[194:201], v[90:93], v192, v192 op_sel_hi:[0,0,0]
	v_mfma_scale_f32_16x16x128_f8f6f4 v[78:81], v[2:9], v[202:209], v[78:81], v192, v192 op_sel_hi:[0,0,0]
	v_mfma_scale_f32_16x16x128_f8f6f4 v[74:77], v[10:17], v[202:209], v[74:77], v192, v192 op_sel_hi:[0,0,0]
	v_mfma_scale_f32_16x16x128_f8f6f4 v[62:65], v[2:9], v[210:217], v[62:65], v192, v192 op_sel_hi:[0,0,0]
	v_mfma_scale_f32_16x16x128_f8f6f4 v[58:61], v[10:17], v[210:217], v[58:61], v192, v192 op_sel_hi:[0,0,0]
	v_mfma_scale_f32_16x16x128_f8f6f4 v[46:49], v[2:9], v[218:225], v[46:49], v192, v192 op_sel_hi:[0,0,0]
	v_mfma_scale_f32_16x16x128_f8f6f4 v[42:45], v[10:17], v[218:225], v[42:45], v192, v192 op_sel_hi:[0,0,0]
	s_nop 3
	s_setprio 0
	s_setprio 1
	v_mfma_scale_f32_16x16x128_f8f6f4 v[86:89], v[18:25], v[194:201], v[86:89], v192, v192 op_sel_hi:[0,0,0]
	v_mfma_scale_f32_16x16x128_f8f6f4 v[82:85], v[26:33], v[194:201], v[82:85], v192, v192 op_sel_hi:[0,0,0]
	v_mfma_scale_f32_16x16x128_f8f6f4 v[70:73], v[18:25], v[202:209], v[70:73], v192, v192 op_sel_hi:[0,0,0]
	v_mfma_scale_f32_16x16x128_f8f6f4 v[66:69], v[26:33], v[202:209], v[66:69], v192, v192 op_sel_hi:[0,0,0]
	v_mfma_scale_f32_16x16x128_f8f6f4 v[54:57], v[18:25], v[210:217], v[54:57], v192, v192 op_sel_hi:[0,0,0]
	v_mfma_scale_f32_16x16x128_f8f6f4 v[50:53], v[26:33], v[210:217], v[50:53], v192, v192 op_sel_hi:[0,0,0]
	v_mfma_scale_f32_16x16x128_f8f6f4 v[38:41], v[18:25], v[218:225], v[38:41], v192, v192 op_sel_hi:[0,0,0]
	v_mfma_scale_f32_16x16x128_f8f6f4 v[34:37], v[26:33], v[218:225], v[34:37], v192, v192 op_sel_hi:[0,0,0]
	s_setprio 0
	s_barrier
	s_add_i32 s68, s68, 2
	s_add_u32 s23, s23, 0x10000
	s_addc_u32 s67, s67, 0
	s_add_u32 s24, s24, 0x10000
	s_addc_u32 s25, s25, 0
	s_cmp_gt_u32 s68, 5
	s_cbranch_scc0 .LBB0_1138
	s_branch .Lfx_33571
	.p2align	6
